# speedup vs baseline: 1.0010x; 1.0010x over previous
_Z8gat_mainPKiPKDF16_PKfS4_Pf:
	s_load_dwordx8 s[24:31], s[0:1], 0x0
	s_load_dwordx2 s[12:13], s[0:1], 0x20
	v_and_b32_e32 v2, 63, v0
	v_readfirstlane_b32 s16, v0
	v_lshlrev_b32_e32 v1, 4, v2
	s_lshr_b32 s16, s16, 6
	s_and_b32 s17, s2, 7
	s_lshr_b32 s18, s2, 3
	s_lshr_b32 s19, s18, 3
	s_add_u32 s19, s19, s18
	s_and_b32 s19, s19, 7
	s_lshr_b32 s20, s16, 2
	s_and_b32 s21, s16, 3
	s_lshl_b32 s22, s16, 16
	s_lshl_b32 s23, s16, 12
	s_waitcnt lgkmcnt(0)
	s_lshl_b32 s3, s17, 24
	s_lshl_b32 s57, s18, 19
	s_add_u32 s3, s3, s57
	s_add_u32 s4, s24, s3
	s_addc_u32 s5, s25, 0
	s_and_b32 s5, s5, 0xffff
	s_mov_b32 s6, 0x80000
	s_mov_b32 s7, 0x20000
	s_lshl_b32 s3, s17, 18
	s_add_u32 s8, s26, s3
	s_addc_u32 s9, s27, 0
	s_and_b32 s9, s9, 0xffff
	s_mov_b32 s10, 0x40000
	s_mov_b32 s11, 0x20000
	s_lshl_b32 s3, s17, 11
	s_lshl_b32 s57, s18, 6
	s_add_u32 s3, s3, s57
	s_lshl_b32 s57, s16, 3
	s_add_u32 s3, s3, s57
	s_lshl_b32 s3, s3, 2
	s_add_u32 s28, s28, s3
	s_addc_u32 s29, s29, 0
	v_and_b32_e32 v36, 7, v0
	v_lshlrev_b32_e32 v36, 2, v36
	global_load_dword v37, v36, s[28:29]
	s_lshl_b32 s3, s17, 13
	s_add_u32 s30, s30, s3
	s_addc_u32 s31, s31, 0
	v_lshlrev_b32_e32 v38, 4, v0
	global_load_dwordx4 v[24:27], v38, s[30:31]
	s_add_u32 s3, s19, 0
	s_and_b32 s3, s3, 7
	s_lshl_b32 s57, s3, 10
	s_add_u32 s48, s57, s22
	s_add_u32 s49, s48, 0x2000
	s_add_u32 s50, s48, 0x4000
	s_add_u32 s51, s48, 0x6000
	s_add_u32 s52, s48, 0x8000
	s_add_u32 s53, s48, 0xa000
	s_add_u32 s54, s48, 0xc000
	s_add_u32 s55, s48, 0xe000
	s_lshl_b32 s56, s3, 15
	s_add_u32 s56, s56, s23
	buffer_load_dwordx4 v[88:91], v1, s[4:7], s48 offen nt
	buffer_load_dwordx4 v[92:95], v1, s[4:7], s49 offen nt
	buffer_load_dwordx4 v[96:99], v1, s[4:7], s50 offen nt
	buffer_load_dwordx4 v[100:103], v1, s[4:7], s51 offen nt
	buffer_load_dwordx4 v[104:107], v1, s[4:7], s52 offen nt
	buffer_load_dwordx4 v[108:111], v1, s[4:7], s53 offen nt
	buffer_load_dwordx4 v[112:115], v1, s[4:7], s54 offen nt
	buffer_load_dwordx4 v[116:119], v1, s[4:7], s55 offen nt
	buffer_load_dwordx4 v[152:155], v1, s[8:11], s56 offen
	buffer_load_dwordx4 v[156:159], v1, s[8:11], s56 offen offset:1024
	buffer_load_dwordx4 v[160:163], v1, s[8:11], s56 offen offset:2048
	buffer_load_dwordx4 v[164:167], v1, s[8:11], s56 offen offset:3072
	s_mul_i32 s3, s16, 0x1080
	v_lshlrev_b32_e32 v3, 3, v2
	v_add_u32_e32 v3, s3, v3
	v_add_u32_e32 v4, 0x840, v3
	v_add_u32_e32 v5, 0x8400, v3
	v_add_u32_e32 v6, 0x8400, v4
	v_and_b32_e32 v36, 31, v2
	v_mul_u32_u24_e32 v36, 0x210, v36
	v_lshrrev_b32_e32 v38, 5, v2
	v_lshlrev_b32_e32 v38, 4, v38
	v_add_u32_e32 v7, v36, v38
	s_mul_i32 s3, s20, 0x4200
	s_lshl_b32 s57, s21, 7
	s_add_u32 s3, s3, s57
	v_add_u32_e32 v7, s3, v7
	s_lshl_b32 s3, s21, 13
	s_add_u32 s3, s3, 0x14800
	v_add_u32_e32 v8, s3, v1
	s_add_u32 s3, s23, 0x14800
	v_add_u32_e32 v9, s3, v1
	v_add_u32_e32 v10, 0x10800, v1
	v_mov_b32_e32 v12, 0x3c003c00
	v_mov_b32_e32 v13, 0x3c003c00
	v_mov_b32_e32 v14, 0x3c003c00
	v_mov_b32_e32 v15, 0x3c003c00
	v_mov_b32_e32 v40, 0
	v_mov_b32_e32 v41, 0
	v_mov_b32_e32 v42, 0
	v_mov_b32_e32 v43, 0
	v_mov_b32_e32 v44, 0
	v_mov_b32_e32 v45, 0
	v_mov_b32_e32 v46, 0
	v_mov_b32_e32 v47, 0
	v_mov_b32_e32 v48, 0
	v_mov_b32_e32 v49, 0
	v_mov_b32_e32 v50, 0
	v_mov_b32_e32 v51, 0
	v_mov_b32_e32 v52, 0
	v_mov_b32_e32 v53, 0
	v_mov_b32_e32 v54, 0
	v_mov_b32_e32 v55, 0
	v_mov_b32_e32 v56, 0
	v_mov_b32_e32 v57, 0
	v_mov_b32_e32 v58, 0
	v_mov_b32_e32 v59, 0
	v_mov_b32_e32 v60, 0
	v_mov_b32_e32 v61, 0
	v_mov_b32_e32 v62, 0
	v_mov_b32_e32 v63, 0
	v_mov_b32_e32 v64, 0
	v_mov_b32_e32 v65, 0
	v_mov_b32_e32 v66, 0
	v_mov_b32_e32 v67, 0
	v_mov_b32_e32 v68, 0
	v_mov_b32_e32 v69, 0
	v_mov_b32_e32 v70, 0
	v_mov_b32_e32 v71, 0
	v_mov_b32_e32 v72, 0
	v_mov_b32_e32 v73, 0
	v_mov_b32_e32 v74, 0
	v_mov_b32_e32 v75, 0
	v_mov_b32_e32 v76, 0
	v_mov_b32_e32 v77, 0
	v_mov_b32_e32 v78, 0
	v_mov_b32_e32 v79, 0
	v_mov_b32_e32 v80, 0
	v_mov_b32_e32 v81, 0
	v_mov_b32_e32 v82, 0
	v_mov_b32_e32 v83, 0
	v_mov_b32_e32 v84, 0
	v_mov_b32_e32 v85, 0
	v_mov_b32_e32 v86, 0
	v_mov_b32_e32 v87, 0
	s_lshl_b32 s3, s17, 11
	s_lshl_b32 s57, s18, 6
	s_add_u32 s3, s3, s57
	s_lshl_b32 s57, s20, 5
	s_add_u32 s3, s3, s57
	s_lshl_b32 s57, s21, 3
	s_add_u32 s3, s3, s57
	s_lshl_b32 s3, s3, 8
	s_add_u32 s12, s12, s3
	s_addc_u32 s13, s13, 0
	s_waitcnt vmcnt(12)
	v_max_f32_e32 v28, v24, v25
	v_max3_f32 v28, v28, v26, v27
	v_lshlrev_b32_e32 v29, 2, v2
	v_xor_b32_e32 v30, 4, v29
	ds_bpermute_b32 v31, v30, v28
	s_waitcnt lgkmcnt(0)
	v_max_f32_e32 v28, v28, v31
	v_xor_b32_e32 v30, 8, v29
	ds_bpermute_b32 v31, v30, v28
	s_waitcnt lgkmcnt(0)
	v_max_f32_e32 v28, v28, v31
	v_xor_b32_e32 v30, 16, v29
	ds_bpermute_b32 v31, v30, v28
	s_waitcnt lgkmcnt(0)
	v_max_f32_e32 v28, v28, v31
	v_xor_b32_e32 v30, 32, v29
	ds_bpermute_b32 v31, v30, v28
	s_waitcnt lgkmcnt(0)
	v_max_f32_e32 v28, v28, v31
	v_xor_b32_e32 v30, 64, v29
	ds_bpermute_b32 v31, v30, v28
	s_waitcnt lgkmcnt(0)
	v_max_f32_e32 v28, v28, v31
	v_xor_b32_e32 v30, 128, v29
	ds_bpermute_b32 v31, v30, v28
	s_waitcnt lgkmcnt(0)
	v_max_f32_e32 v28, v28, v31
	s_lshl_b32 s3, s16, 2
	s_add_u32 s3, s3, 0x24800
	v_mov_b32_e32 v30, s3
	ds_write_b32 v30, v28
	s_waitcnt lgkmcnt(0)
	s_barrier
	v_mov_b32_e32 v30, 0x24800
	ds_read_b128 v[32:35], v30
	ds_read_b128 v[16:19], v30 offset:16
	s_waitcnt lgkmcnt(0)
	v_max3_f32 v28, v32, v33, v34
	v_max3_f32 v28, v28, v35, v16
	v_max3_f32 v28, v28, v17, v18
	v_max_f32_e32 v28, v28, v19
	v_sub_f32_e32 v16, v24, v28
	v_sub_f32_e32 v17, v25, v28
	v_sub_f32_e32 v18, v26, v28
	v_sub_f32_e32 v19, v27, v28
	v_mul_f32_e32 v20, 0x3e4ccccd, v16
	v_mul_f32_e32 v21, 0x3e4ccccd, v17
	v_mul_f32_e32 v22, 0x3e4ccccd, v18
	v_mul_f32_e32 v23, 0x3e4ccccd, v19
	v_exp_f32_e32 v16, v16
	v_exp_f32_e32 v17, v17
	v_exp_f32_e32 v18, v18
	v_exp_f32_e32 v19, v19
	v_exp_f32_e32 v20, v20
	v_exp_f32_e32 v21, v21
	v_exp_f32_e32 v22, v22
	v_exp_f32_e32 v23, v23
	v_lshlrev_b32_e32 v30, 4, v0
	v_add_u32_e32 v30, 0x10800, v30
	ds_write_b128 v30, v[16:19]
	ds_write_b128 v30, v[20:23] offset:8192
	v_add_f32_e32 v36, v37, v28
	v_mul_f32_e32 v38, 0x3e4ccccd, v36
	v_max_f32_e32 v39, v36, v38
	v_sub_f32_e32 v36, v36, v39
	v_sub_f32_e32 v38, v38, v39
	v_add_f32_e32 v36, 0x41600000, v36
	v_add_f32_e32 v38, 0x41600000, v38
	v_exp_f32_e32 v36, v36
	v_exp_f32_e32 v38, v38
	s_nop 1
	v_readlane_b32 s32, v36, 0
	v_readlane_b32 s33, v36, 1
	v_readlane_b32 s34, v36, 2
	v_readlane_b32 s35, v36, 3
	v_readlane_b32 s36, v36, 4
	v_readlane_b32 s37, v36, 5
	v_readlane_b32 s38, v36, 6
	v_readlane_b32 s39, v36, 7
	v_readlane_b32 s40, v38, 0
	v_readlane_b32 s41, v38, 1
	v_readlane_b32 s42, v38, 2
	v_readlane_b32 s43, v38, 3
	v_readlane_b32 s44, v38, 4
	v_readlane_b32 s45, v38, 5
	v_readlane_b32 s46, v38, 6
	v_readlane_b32 s47, v38, 7
	s_waitcnt lgkmcnt(0)
	s_barrier
	s_lshl_b32 s3, s19, 10
	v_add_u32_e32 v11, s3, v10
	ds_read_b128 v[16:19], v11
	ds_read_b128 v[20:23], v11 offset:8192
	s_waitcnt lgkmcnt(0)
	s_add_u32 s3, s19, 1
	s_and_b32 s3, s3, 7
	s_lshl_b32 s57, s3, 10
	s_add_u32 s48, s57, s22
	s_add_u32 s49, s48, 0x2000
	s_add_u32 s50, s48, 0x4000
	s_add_u32 s51, s48, 0x6000
	s_add_u32 s52, s48, 0x8000
	s_add_u32 s53, s48, 0xa000
	s_add_u32 s54, s48, 0xc000
	s_add_u32 s55, s48, 0xe000
	s_lshl_b32 s56, s3, 15
	s_add_u32 s56, s56, s23
	buffer_load_dwordx4 v[120:123], v1, s[4:7], s48 offen nt
	buffer_load_dwordx4 v[124:127], v1, s[4:7], s49 offen nt
	buffer_load_dwordx4 v[128:131], v1, s[4:7], s50 offen nt
	buffer_load_dwordx4 v[132:135], v1, s[4:7], s51 offen nt
	buffer_load_dwordx4 v[136:139], v1, s[4:7], s52 offen nt
	buffer_load_dwordx4 v[140:143], v1, s[4:7], s53 offen nt
	buffer_load_dwordx4 v[144:147], v1, s[4:7], s54 offen nt
	buffer_load_dwordx4 v[148:151], v1, s[4:7], s55 offen nt
	buffer_load_dwordx4 v[168:171], v1, s[8:11], s56 offen
	buffer_load_dwordx4 v[172:175], v1, s[8:11], s56 offen offset:1024
	buffer_load_dwordx4 v[176:179], v1, s[8:11], s56 offen offset:2048
	buffer_load_dwordx4 v[180:183], v1, s[8:11], s56 offen offset:3072
	s_waitcnt vmcnt(12)
	v_pk_mul_f32 v[24:25], v[16:17], s[32:33] op_sel_hi:[1,0]
	v_pk_mul_f32 v[26:27], v[18:19], s[32:33] op_sel_hi:[1,0]
	v_pk_mul_f32 v[28:29], v[20:21], s[40:41] op_sel_hi:[1,0]
	v_pk_mul_f32 v[30:31], v[22:23], s[40:41] op_sel_hi:[1,0]
	v_cmp_lt_i32_e64 s[60:61], 0, v88
	v_cmp_lt_i32_e64 s[62:63], 0, v89
	v_cmp_lt_i32_e64 s[64:65], 0, v90
	v_cmp_lt_i32_e64 s[66:67], 0, v91
	v_max_f32_e32 v24, v24, v28
	v_max_f32_e32 v25, v25, v29
	v_max_f32_e32 v26, v26, v30
	v_max_f32_e32 v27, v27, v31
	v_cndmask_b32_e64 v24, 0, v24, s[60:61]
	v_cndmask_b32_e64 v25, 0, v25, s[62:63]
	v_cndmask_b32_e64 v26, 0, v26, s[64:65]
	v_cndmask_b32_e64 v27, 0, v27, s[66:67]
	v_cvt_pkrtz_f16_f32 v32, v24, v25
	v_cvt_pkrtz_f16_f32 v33, v26, v27
	v_pk_mul_f32 v[24:25], v[16:17], s[32:33] op_sel:[0,1] op_sel_hi:[1,1]
	v_pk_mul_f32 v[26:27], v[18:19], s[32:33] op_sel:[0,1] op_sel_hi:[1,1]
	v_pk_mul_f32 v[28:29], v[20:21], s[40:41] op_sel:[0,1] op_sel_hi:[1,1]
	v_pk_mul_f32 v[30:31], v[22:23], s[40:41] op_sel:[0,1] op_sel_hi:[1,1]
	v_cmp_lt_i32_e64 s[60:61], 0, v92
	v_cmp_lt_i32_e64 s[62:63], 0, v93
	v_cmp_lt_i32_e64 s[64:65], 0, v94
	v_cmp_lt_i32_e64 s[66:67], 0, v95
	v_max_f32_e32 v24, v24, v28
	v_max_f32_e32 v25, v25, v29
	v_max_f32_e32 v26, v26, v30
	v_max_f32_e32 v27, v27, v31
	v_cndmask_b32_e64 v24, 0, v24, s[60:61]
	v_cndmask_b32_e64 v25, 0, v25, s[62:63]
	v_cndmask_b32_e64 v26, 0, v26, s[64:65]
	v_cndmask_b32_e64 v27, 0, v27, s[66:67]
	v_cvt_pkrtz_f16_f32 v34, v24, v25
	v_cvt_pkrtz_f16_f32 v35, v26, v27
	ds_write2_b64 v3, v[32:33], v[34:35] offset0:0 offset1:66
	v_pk_mul_f32 v[24:25], v[16:17], s[34:35] op_sel_hi:[1,0]
	v_pk_mul_f32 v[26:27], v[18:19], s[34:35] op_sel_hi:[1,0]
	v_pk_mul_f32 v[28:29], v[20:21], s[42:43] op_sel_hi:[1,0]
	v_pk_mul_f32 v[30:31], v[22:23], s[42:43] op_sel_hi:[1,0]
	v_cmp_lt_i32_e64 s[60:61], 0, v96
	v_cmp_lt_i32_e64 s[62:63], 0, v97
	v_cmp_lt_i32_e64 s[64:65], 0, v98
	v_cmp_lt_i32_e64 s[66:67], 0, v99
	v_max_f32_e32 v24, v24, v28
	v_max_f32_e32 v25, v25, v29
	v_max_f32_e32 v26, v26, v30
	v_max_f32_e32 v27, v27, v31
	v_cndmask_b32_e64 v24, 0, v24, s[60:61]
	v_cndmask_b32_e64 v25, 0, v25, s[62:63]
	v_cndmask_b32_e64 v26, 0, v26, s[64:65]
	v_cndmask_b32_e64 v27, 0, v27, s[66:67]
	v_cvt_pkrtz_f16_f32 v32, v24, v25
	v_cvt_pkrtz_f16_f32 v33, v26, v27
	v_pk_mul_f32 v[24:25], v[16:17], s[34:35] op_sel:[0,1] op_sel_hi:[1,1]
	v_pk_mul_f32 v[26:27], v[18:19], s[34:35] op_sel:[0,1] op_sel_hi:[1,1]
	v_pk_mul_f32 v[28:29], v[20:21], s[42:43] op_sel:[0,1] op_sel_hi:[1,1]
	v_pk_mul_f32 v[30:31], v[22:23], s[42:43] op_sel:[0,1] op_sel_hi:[1,1]
	v_cmp_lt_i32_e64 s[60:61], 0, v100
	v_cmp_lt_i32_e64 s[62:63], 0, v101
	v_cmp_lt_i32_e64 s[64:65], 0, v102
	v_cmp_lt_i32_e64 s[66:67], 0, v103
	v_max_f32_e32 v24, v24, v28
	v_max_f32_e32 v25, v25, v29
	v_max_f32_e32 v26, v26, v30
	v_max_f32_e32 v27, v27, v31
	v_cndmask_b32_e64 v24, 0, v24, s[60:61]
	v_cndmask_b32_e64 v25, 0, v25, s[62:63]
	v_cndmask_b32_e64 v26, 0, v26, s[64:65]
	v_cndmask_b32_e64 v27, 0, v27, s[66:67]
	v_cvt_pkrtz_f16_f32 v34, v24, v25
	v_cvt_pkrtz_f16_f32 v35, v26, v27
	ds_write2_b64 v3, v[32:33], v[34:35] offset0:132 offset1:198
	v_pk_mul_f32 v[24:25], v[16:17], s[36:37] op_sel_hi:[1,0]
	v_pk_mul_f32 v[26:27], v[18:19], s[36:37] op_sel_hi:[1,0]
	v_pk_mul_f32 v[28:29], v[20:21], s[44:45] op_sel_hi:[1,0]
	v_pk_mul_f32 v[30:31], v[22:23], s[44:45] op_sel_hi:[1,0]
	v_cmp_lt_i32_e64 s[60:61], 0, v104
	v_cmp_lt_i32_e64 s[62:63], 0, v105
	v_cmp_lt_i32_e64 s[64:65], 0, v106
	v_cmp_lt_i32_e64 s[66:67], 0, v107
	v_max_f32_e32 v24, v24, v28
	v_max_f32_e32 v25, v25, v29
	v_max_f32_e32 v26, v26, v30
	v_max_f32_e32 v27, v27, v31
	v_cndmask_b32_e64 v24, 0, v24, s[60:61]
	v_cndmask_b32_e64 v25, 0, v25, s[62:63]
	v_cndmask_b32_e64 v26, 0, v26, s[64:65]
	v_cndmask_b32_e64 v27, 0, v27, s[66:67]
	v_cvt_pkrtz_f16_f32 v32, v24, v25
	v_cvt_pkrtz_f16_f32 v33, v26, v27
	v_pk_mul_f32 v[24:25], v[16:17], s[36:37] op_sel:[0,1] op_sel_hi:[1,1]
	v_pk_mul_f32 v[26:27], v[18:19], s[36:37] op_sel:[0,1] op_sel_hi:[1,1]
	v_pk_mul_f32 v[28:29], v[20:21], s[44:45] op_sel:[0,1] op_sel_hi:[1,1]
	v_pk_mul_f32 v[30:31], v[22:23], s[44:45] op_sel:[0,1] op_sel_hi:[1,1]
	v_cmp_lt_i32_e64 s[60:61], 0, v108
	v_cmp_lt_i32_e64 s[62:63], 0, v109
	v_cmp_lt_i32_e64 s[64:65], 0, v110
	v_cmp_lt_i32_e64 s[66:67], 0, v111
	v_max_f32_e32 v24, v24, v28
	v_max_f32_e32 v25, v25, v29
	v_max_f32_e32 v26, v26, v30
	v_max_f32_e32 v27, v27, v31
	v_cndmask_b32_e64 v24, 0, v24, s[60:61]
	v_cndmask_b32_e64 v25, 0, v25, s[62:63]
	v_cndmask_b32_e64 v26, 0, v26, s[64:65]
	v_cndmask_b32_e64 v27, 0, v27, s[66:67]
	v_cvt_pkrtz_f16_f32 v34, v24, v25
	v_cvt_pkrtz_f16_f32 v35, v26, v27
	ds_write2_b64 v4, v[32:33], v[34:35] offset0:0 offset1:66
	v_pk_mul_f32 v[24:25], v[16:17], s[38:39] op_sel_hi:[1,0]
	v_pk_mul_f32 v[26:27], v[18:19], s[38:39] op_sel_hi:[1,0]
	v_pk_mul_f32 v[28:29], v[20:21], s[46:47] op_sel_hi:[1,0]
	v_pk_mul_f32 v[30:31], v[22:23], s[46:47] op_sel_hi:[1,0]
	v_cmp_lt_i32_e64 s[60:61], 0, v112
	v_cmp_lt_i32_e64 s[62:63], 0, v113
	v_cmp_lt_i32_e64 s[64:65], 0, v114
	v_cmp_lt_i32_e64 s[66:67], 0, v115
	v_max_f32_e32 v24, v24, v28
	v_max_f32_e32 v25, v25, v29
	v_max_f32_e32 v26, v26, v30
	v_max_f32_e32 v27, v27, v31
	v_cndmask_b32_e64 v24, 0, v24, s[60:61]
	v_cndmask_b32_e64 v25, 0, v25, s[62:63]
	v_cndmask_b32_e64 v26, 0, v26, s[64:65]
	v_cndmask_b32_e64 v27, 0, v27, s[66:67]
	v_cvt_pkrtz_f16_f32 v32, v24, v25
	v_cvt_pkrtz_f16_f32 v33, v26, v27
	v_pk_mul_f32 v[24:25], v[16:17], s[38:39] op_sel:[0,1] op_sel_hi:[1,1]
	v_pk_mul_f32 v[26:27], v[18:19], s[38:39] op_sel:[0,1] op_sel_hi:[1,1]
	v_pk_mul_f32 v[28:29], v[20:21], s[46:47] op_sel:[0,1] op_sel_hi:[1,1]
	v_pk_mul_f32 v[30:31], v[22:23], s[46:47] op_sel:[0,1] op_sel_hi:[1,1]
	v_cmp_lt_i32_e64 s[60:61], 0, v116
	v_cmp_lt_i32_e64 s[62:63], 0, v117
	v_cmp_lt_i32_e64 s[64:65], 0, v118
	v_cmp_lt_i32_e64 s[66:67], 0, v119
	v_max_f32_e32 v24, v24, v28
	v_max_f32_e32 v25, v25, v29
	v_max_f32_e32 v26, v26, v30
	v_max_f32_e32 v27, v27, v31
	v_cndmask_b32_e64 v24, 0, v24, s[60:61]
	v_cndmask_b32_e64 v25, 0, v25, s[62:63]
	v_cndmask_b32_e64 v26, 0, v26, s[64:65]
	v_cndmask_b32_e64 v27, 0, v27, s[66:67]
	v_cvt_pkrtz_f16_f32 v34, v24, v25
	v_cvt_pkrtz_f16_f32 v35, v26, v27
	ds_write2_b64 v4, v[32:33], v[34:35] offset0:132 offset1:198
	ds_write_b128 v9, v[152:155] offset:0
	ds_write_b128 v9, v[156:159] offset:1024
	ds_write_b128 v9, v[160:163] offset:2048
	ds_write_b128 v9, v[164:167] offset:3072
	s_add_u32 s3, s19, 1
	s_and_b32 s3, s3, 7
	s_lshl_b32 s3, s3, 10
	v_add_u32_e32 v11, s3, v10
	ds_read_b128 v[16:19], v11
	ds_read_b128 v[20:23], v11 offset:8192
	s_waitcnt lgkmcnt(0)
	s_barrier
	ds_read_b128 v[184:187], v7 offset:0
	ds_read_b128 v[200:203], v8 offset:0
	ds_read_b128 v[204:207], v8 offset:1024
	ds_read_b128 v[188:191], v7 offset:32
	ds_read_b128 v[208:211], v8 offset:2048
	ds_read_b128 v[212:215], v8 offset:3072
	ds_read_b128 v[192:195], v7 offset:64
	ds_read_b128 v[216:219], v8 offset:4096
	ds_read_b128 v[220:223], v8 offset:5120
	ds_read_b128 v[196:199], v7 offset:96
	ds_read_b128 v[224:227], v8 offset:6144
	ds_read_b128 v[228:231], v8 offset:7168
	s_add_u32 s3, s19, 2
	s_and_b32 s3, s3, 7
	s_lshl_b32 s57, s3, 10
	s_add_u32 s48, s57, s22
	s_add_u32 s49, s48, 0x2000
	s_add_u32 s50, s48, 0x4000
	s_add_u32 s51, s48, 0x6000
	s_add_u32 s52, s48, 0x8000
	s_add_u32 s53, s48, 0xa000
	s_add_u32 s54, s48, 0xc000
	s_add_u32 s55, s48, 0xe000
	s_lshl_b32 s56, s3, 15
	s_add_u32 s56, s56, s23
	buffer_load_dwordx4 v[88:91], v1, s[4:7], s48 offen nt
	buffer_load_dwordx4 v[92:95], v1, s[4:7], s49 offen nt
	buffer_load_dwordx4 v[96:99], v1, s[4:7], s50 offen nt
	buffer_load_dwordx4 v[100:103], v1, s[4:7], s51 offen nt
	buffer_load_dwordx4 v[104:107], v1, s[4:7], s52 offen nt
	buffer_load_dwordx4 v[108:111], v1, s[4:7], s53 offen nt
	buffer_load_dwordx4 v[112:115], v1, s[4:7], s54 offen nt
	buffer_load_dwordx4 v[116:119], v1, s[4:7], s55 offen nt
	buffer_load_dwordx4 v[152:155], v1, s[8:11], s56 offen
	buffer_load_dwordx4 v[156:159], v1, s[8:11], s56 offen offset:1024
	buffer_load_dwordx4 v[160:163], v1, s[8:11], s56 offen offset:2048
	buffer_load_dwordx4 v[164:167], v1, s[8:11], s56 offen offset:3072
	s_waitcnt vmcnt(12)
	v_pk_mul_f32 v[24:25], v[16:17], s[32:33] op_sel_hi:[1,0]
	v_pk_mul_f32 v[26:27], v[18:19], s[32:33] op_sel_hi:[1,0]
	v_pk_mul_f32 v[28:29], v[20:21], s[40:41] op_sel_hi:[1,0]
	v_pk_mul_f32 v[30:31], v[22:23], s[40:41] op_sel_hi:[1,0]
	v_cmp_lt_i32_e64 s[60:61], 0, v120
	v_cmp_lt_i32_e64 s[62:63], 0, v121
	v_cmp_lt_i32_e64 s[64:65], 0, v122
	v_cmp_lt_i32_e64 s[66:67], 0, v123
	v_max_f32_e32 v24, v24, v28
	v_max_f32_e32 v25, v25, v29
	v_max_f32_e32 v26, v26, v30
	v_max_f32_e32 v27, v27, v31
	v_cndmask_b32_e64 v24, 0, v24, s[60:61]
	v_cndmask_b32_e64 v25, 0, v25, s[62:63]
	v_cndmask_b32_e64 v26, 0, v26, s[64:65]
	v_cndmask_b32_e64 v27, 0, v27, s[66:67]
	v_cvt_pkrtz_f16_f32 v32, v24, v25
	v_cvt_pkrtz_f16_f32 v33, v26, v27
	s_waitcnt lgkmcnt(0)
	v_pk_mul_f32 v[24:25], v[16:17], s[32:33] op_sel:[0,1] op_sel_hi:[1,1]
	v_pk_mul_f32 v[26:27], v[18:19], s[32:33] op_sel:[0,1] op_sel_hi:[1,1]
	v_pk_mul_f32 v[28:29], v[20:21], s[40:41] op_sel:[0,1] op_sel_hi:[1,1]
	v_pk_mul_f32 v[30:31], v[22:23], s[40:41] op_sel:[0,1] op_sel_hi:[1,1]
	v_mfma_f32_32x32x16_f16 v[40:55], v[184:187], v[200:203], v[40:55]
	v_cmp_lt_i32_e64 s[60:61], 0, v124
	v_cmp_lt_i32_e64 s[62:63], 0, v125
	v_cmp_lt_i32_e64 s[64:65], 0, v126
	v_cmp_lt_i32_e64 s[66:67], 0, v127
	v_max_f32_e32 v24, v24, v28
	v_max_f32_e32 v25, v25, v29
	v_max_f32_e32 v26, v26, v30
	v_max_f32_e32 v27, v27, v31
	v_cndmask_b32_e64 v24, 0, v24, s[60:61]
	v_cndmask_b32_e64 v25, 0, v25, s[62:63]
	v_cndmask_b32_e64 v26, 0, v26, s[64:65]
	v_cndmask_b32_e64 v27, 0, v27, s[66:67]
	v_mfma_f32_32x32x16_f16 v[56:71], v[184:187], v[204:207], v[56:71]
	v_cvt_pkrtz_f16_f32 v34, v24, v25
	v_cvt_pkrtz_f16_f32 v35, v26, v27
	ds_write2_b64 v5, v[32:33], v[34:35] offset0:0 offset1:66
	v_pk_mul_f32 v[24:25], v[16:17], s[34:35] op_sel_hi:[1,0]
	v_pk_mul_f32 v[26:27], v[18:19], s[34:35] op_sel_hi:[1,0]
	v_pk_mul_f32 v[28:29], v[20:21], s[42:43] op_sel_hi:[1,0]
	v_pk_mul_f32 v[30:31], v[22:23], s[42:43] op_sel_hi:[1,0]
	v_mfma_f32_32x32x16_f16 v[72:87], v[184:187], v[12:15], v[72:87]
	v_cmp_lt_i32_e64 s[60:61], 0, v128
	v_cmp_lt_i32_e64 s[62:63], 0, v129
	v_cmp_lt_i32_e64 s[64:65], 0, v130
	v_cmp_lt_i32_e64 s[66:67], 0, v131
	v_max_f32_e32 v24, v24, v28
	v_max_f32_e32 v25, v25, v29
	v_max_f32_e32 v26, v26, v30
	v_max_f32_e32 v27, v27, v31
	v_cndmask_b32_e64 v24, 0, v24, s[60:61]
	v_cndmask_b32_e64 v25, 0, v25, s[62:63]
	v_cndmask_b32_e64 v26, 0, v26, s[64:65]
	v_cndmask_b32_e64 v27, 0, v27, s[66:67]
	v_mfma_f32_32x32x16_f16 v[40:55], v[188:191], v[208:211], v[40:55]
	v_cvt_pkrtz_f16_f32 v32, v24, v25
	v_cvt_pkrtz_f16_f32 v33, v26, v27
	v_pk_mul_f32 v[24:25], v[16:17], s[34:35] op_sel:[0,1] op_sel_hi:[1,1]
	v_pk_mul_f32 v[26:27], v[18:19], s[34:35] op_sel:[0,1] op_sel_hi:[1,1]
	v_pk_mul_f32 v[28:29], v[20:21], s[42:43] op_sel:[0,1] op_sel_hi:[1,1]
	v_pk_mul_f32 v[30:31], v[22:23], s[42:43] op_sel:[0,1] op_sel_hi:[1,1]
	v_mfma_f32_32x32x16_f16 v[56:71], v[188:191], v[212:215], v[56:71]
	v_cmp_lt_i32_e64 s[60:61], 0, v132
	v_cmp_lt_i32_e64 s[62:63], 0, v133
	v_cmp_lt_i32_e64 s[64:65], 0, v134
	v_cmp_lt_i32_e64 s[66:67], 0, v135
	v_max_f32_e32 v24, v24, v28
	v_max_f32_e32 v25, v25, v29
	v_max_f32_e32 v26, v26, v30
	v_max_f32_e32 v27, v27, v31
	v_cndmask_b32_e64 v24, 0, v24, s[60:61]
	v_cndmask_b32_e64 v25, 0, v25, s[62:63]
	v_cndmask_b32_e64 v26, 0, v26, s[64:65]
	v_cndmask_b32_e64 v27, 0, v27, s[66:67]
	v_mfma_f32_32x32x16_f16 v[72:87], v[188:191], v[12:15], v[72:87]
	v_cvt_pkrtz_f16_f32 v34, v24, v25
	v_cvt_pkrtz_f16_f32 v35, v26, v27
	ds_write2_b64 v5, v[32:33], v[34:35] offset0:132 offset1:198
	v_pk_mul_f32 v[24:25], v[16:17], s[36:37] op_sel_hi:[1,0]
	v_pk_mul_f32 v[26:27], v[18:19], s[36:37] op_sel_hi:[1,0]
	v_pk_mul_f32 v[28:29], v[20:21], s[44:45] op_sel_hi:[1,0]
	v_pk_mul_f32 v[30:31], v[22:23], s[44:45] op_sel_hi:[1,0]
	v_mfma_f32_32x32x16_f16 v[40:55], v[192:195], v[216:219], v[40:55]
	v_cmp_lt_i32_e64 s[60:61], 0, v136
	v_cmp_lt_i32_e64 s[62:63], 0, v137
	v_cmp_lt_i32_e64 s[64:65], 0, v138
	v_cmp_lt_i32_e64 s[66:67], 0, v139
	v_max_f32_e32 v24, v24, v28
	v_max_f32_e32 v25, v25, v29
	v_max_f32_e32 v26, v26, v30
	v_max_f32_e32 v27, v27, v31
	v_cndmask_b32_e64 v24, 0, v24, s[60:61]
	v_cndmask_b32_e64 v25, 0, v25, s[62:63]
	v_cndmask_b32_e64 v26, 0, v26, s[64:65]
	v_cndmask_b32_e64 v27, 0, v27, s[66:67]
	v_mfma_f32_32x32x16_f16 v[56:71], v[192:195], v[220:223], v[56:71]
	v_cvt_pkrtz_f16_f32 v32, v24, v25
	v_cvt_pkrtz_f16_f32 v33, v26, v27
	v_pk_mul_f32 v[24:25], v[16:17], s[36:37] op_sel:[0,1] op_sel_hi:[1,1]
	v_pk_mul_f32 v[26:27], v[18:19], s[36:37] op_sel:[0,1] op_sel_hi:[1,1]
	v_pk_mul_f32 v[28:29], v[20:21], s[44:45] op_sel:[0,1] op_sel_hi:[1,1]
	v_pk_mul_f32 v[30:31], v[22:23], s[44:45] op_sel:[0,1] op_sel_hi:[1,1]
	v_mfma_f32_32x32x16_f16 v[72:87], v[192:195], v[12:15], v[72:87]
	v_cmp_lt_i32_e64 s[60:61], 0, v140
	v_cmp_lt_i32_e64 s[62:63], 0, v141
	v_cmp_lt_i32_e64 s[64:65], 0, v142
	v_cmp_lt_i32_e64 s[66:67], 0, v143
	v_max_f32_e32 v24, v24, v28
	v_max_f32_e32 v25, v25, v29
	v_max_f32_e32 v26, v26, v30
	v_max_f32_e32 v27, v27, v31
	v_cndmask_b32_e64 v24, 0, v24, s[60:61]
	v_cndmask_b32_e64 v25, 0, v25, s[62:63]
	v_cndmask_b32_e64 v26, 0, v26, s[64:65]
	v_cndmask_b32_e64 v27, 0, v27, s[66:67]
	v_mfma_f32_32x32x16_f16 v[40:55], v[196:199], v[224:227], v[40:55]
	v_cvt_pkrtz_f16_f32 v34, v24, v25
	v_cvt_pkrtz_f16_f32 v35, v26, v27
	ds_write2_b64 v6, v[32:33], v[34:35] offset0:0 offset1:66
	v_pk_mul_f32 v[24:25], v[16:17], s[38:39] op_sel_hi:[1,0]
	v_pk_mul_f32 v[26:27], v[18:19], s[38:39] op_sel_hi:[1,0]
	v_pk_mul_f32 v[28:29], v[20:21], s[46:47] op_sel_hi:[1,0]
	v_pk_mul_f32 v[30:31], v[22:23], s[46:47] op_sel_hi:[1,0]
	v_mfma_f32_32x32x16_f16 v[56:71], v[196:199], v[228:231], v[56:71]
	v_cmp_lt_i32_e64 s[60:61], 0, v144
	v_cmp_lt_i32_e64 s[62:63], 0, v145
	v_cmp_lt_i32_e64 s[64:65], 0, v146
	v_cmp_lt_i32_e64 s[66:67], 0, v147
	v_max_f32_e32 v24, v24, v28
	v_max_f32_e32 v25, v25, v29
	v_max_f32_e32 v26, v26, v30
	v_max_f32_e32 v27, v27, v31
	v_cndmask_b32_e64 v24, 0, v24, s[60:61]
	v_cndmask_b32_e64 v25, 0, v25, s[62:63]
	v_cndmask_b32_e64 v26, 0, v26, s[64:65]
	v_cndmask_b32_e64 v27, 0, v27, s[66:67]
	v_cvt_pkrtz_f16_f32 v32, v24, v25
	v_cvt_pkrtz_f16_f32 v33, v26, v27
	v_pk_mul_f32 v[24:25], v[16:17], s[38:39] op_sel:[0,1] op_sel_hi:[1,1]
	v_pk_mul_f32 v[26:27], v[18:19], s[38:39] op_sel:[0,1] op_sel_hi:[1,1]
	v_pk_mul_f32 v[28:29], v[20:21], s[46:47] op_sel:[0,1] op_sel_hi:[1,1]
	v_pk_mul_f32 v[30:31], v[22:23], s[46:47] op_sel:[0,1] op_sel_hi:[1,1]
	v_mfma_f32_32x32x16_f16 v[72:87], v[196:199], v[12:15], v[72:87]
	v_cmp_lt_i32_e64 s[60:61], 0, v148
	v_cmp_lt_i32_e64 s[62:63], 0, v149
	v_cmp_lt_i32_e64 s[64:65], 0, v150
	v_cmp_lt_i32_e64 s[66:67], 0, v151
	v_max_f32_e32 v24, v24, v28
	v_max_f32_e32 v25, v25, v29
	v_max_f32_e32 v26, v26, v30
	v_max_f32_e32 v27, v27, v31
	v_cndmask_b32_e64 v24, 0, v24, s[60:61]
	v_cndmask_b32_e64 v25, 0, v25, s[62:63]
	v_cndmask_b32_e64 v26, 0, v26, s[64:65]
	v_cndmask_b32_e64 v27, 0, v27, s[66:67]
	v_cvt_pkrtz_f16_f32 v34, v24, v25
	v_cvt_pkrtz_f16_f32 v35, v26, v27
	ds_write2_b64 v6, v[32:33], v[34:35] offset0:132 offset1:198
	ds_write_b128 v9, v[168:171] offset:32768
	ds_write_b128 v9, v[172:175] offset:33792
	ds_write_b128 v9, v[176:179] offset:34816
	ds_write_b128 v9, v[180:183] offset:35840
	s_add_u32 s3, s19, 2
	s_and_b32 s3, s3, 7
	s_lshl_b32 s3, s3, 10
	v_add_u32_e32 v11, s3, v10
	ds_read_b128 v[16:19], v11
	ds_read_b128 v[20:23], v11 offset:8192
	s_waitcnt lgkmcnt(0)
	s_barrier
	ds_read_b128 v[184:187], v7 offset:33792
	ds_read_b128 v[200:203], v8 offset:32768
	ds_read_b128 v[204:207], v8 offset:33792
	ds_read_b128 v[188:191], v7 offset:33824
	ds_read_b128 v[208:211], v8 offset:34816
	ds_read_b128 v[212:215], v8 offset:35840
	ds_read_b128 v[192:195], v7 offset:33856
	ds_read_b128 v[216:219], v8 offset:36864
	ds_read_b128 v[220:223], v8 offset:37888
	ds_read_b128 v[196:199], v7 offset:33888
	ds_read_b128 v[224:227], v8 offset:38912
	ds_read_b128 v[228:231], v8 offset:39936
	s_add_u32 s3, s19, 3
	s_and_b32 s3, s3, 7
	s_lshl_b32 s57, s3, 10
	s_add_u32 s48, s57, s22
	s_add_u32 s49, s48, 0x2000
	s_add_u32 s50, s48, 0x4000
	s_add_u32 s51, s48, 0x6000
	s_add_u32 s52, s48, 0x8000
	s_add_u32 s53, s48, 0xa000
	s_add_u32 s54, s48, 0xc000
	s_add_u32 s55, s48, 0xe000
	s_lshl_b32 s56, s3, 15
	s_add_u32 s56, s56, s23
	buffer_load_dwordx4 v[120:123], v1, s[4:7], s48 offen nt
	buffer_load_dwordx4 v[124:127], v1, s[4:7], s49 offen nt
	buffer_load_dwordx4 v[128:131], v1, s[4:7], s50 offen nt
	buffer_load_dwordx4 v[132:135], v1, s[4:7], s51 offen nt
	buffer_load_dwordx4 v[136:139], v1, s[4:7], s52 offen nt
	buffer_load_dwordx4 v[140:143], v1, s[4:7], s53 offen nt
	buffer_load_dwordx4 v[144:147], v1, s[4:7], s54 offen nt
	buffer_load_dwordx4 v[148:151], v1, s[4:7], s55 offen nt
	buffer_load_dwordx4 v[168:171], v1, s[8:11], s56 offen
	buffer_load_dwordx4 v[172:175], v1, s[8:11], s56 offen offset:1024
	buffer_load_dwordx4 v[176:179], v1, s[8:11], s56 offen offset:2048
	buffer_load_dwordx4 v[180:183], v1, s[8:11], s56 offen offset:3072
	s_waitcnt vmcnt(12)
	v_pk_mul_f32 v[24:25], v[16:17], s[32:33] op_sel_hi:[1,0]
	v_pk_mul_f32 v[26:27], v[18:19], s[32:33] op_sel_hi:[1,0]
	v_pk_mul_f32 v[28:29], v[20:21], s[40:41] op_sel_hi:[1,0]
	v_pk_mul_f32 v[30:31], v[22:23], s[40:41] op_sel_hi:[1,0]
	v_cmp_lt_i32_e64 s[60:61], 0, v88
	v_cmp_lt_i32_e64 s[62:63], 0, v89
	v_cmp_lt_i32_e64 s[64:65], 0, v90
	v_cmp_lt_i32_e64 s[66:67], 0, v91
	v_max_f32_e32 v24, v24, v28
	v_max_f32_e32 v25, v25, v29
	v_max_f32_e32 v26, v26, v30
	v_max_f32_e32 v27, v27, v31
	v_cndmask_b32_e64 v24, 0, v24, s[60:61]
	v_cndmask_b32_e64 v25, 0, v25, s[62:63]
	v_cndmask_b32_e64 v26, 0, v26, s[64:65]
	v_cndmask_b32_e64 v27, 0, v27, s[66:67]
	v_cvt_pkrtz_f16_f32 v32, v24, v25
	v_cvt_pkrtz_f16_f32 v33, v26, v27
	s_waitcnt lgkmcnt(0)
	v_pk_mul_f32 v[24:25], v[16:17], s[32:33] op_sel:[0,1] op_sel_hi:[1,1]
	v_pk_mul_f32 v[26:27], v[18:19], s[32:33] op_sel:[0,1] op_sel_hi:[1,1]
	v_pk_mul_f32 v[28:29], v[20:21], s[40:41] op_sel:[0,1] op_sel_hi:[1,1]
	v_pk_mul_f32 v[30:31], v[22:23], s[40:41] op_sel:[0,1] op_sel_hi:[1,1]
	v_mfma_f32_32x32x16_f16 v[40:55], v[184:187], v[200:203], v[40:55]
	v_cmp_lt_i32_e64 s[60:61], 0, v92
	v_cmp_lt_i32_e64 s[62:63], 0, v93
	v_cmp_lt_i32_e64 s[64:65], 0, v94
	v_cmp_lt_i32_e64 s[66:67], 0, v95
	v_max_f32_e32 v24, v24, v28
	v_max_f32_e32 v25, v25, v29
	v_max_f32_e32 v26, v26, v30
	v_max_f32_e32 v27, v27, v31
	v_cndmask_b32_e64 v24, 0, v24, s[60:61]
	v_cndmask_b32_e64 v25, 0, v25, s[62:63]
	v_cndmask_b32_e64 v26, 0, v26, s[64:65]
	v_cndmask_b32_e64 v27, 0, v27, s[66:67]
	v_mfma_f32_32x32x16_f16 v[56:71], v[184:187], v[204:207], v[56:71]
	v_cvt_pkrtz_f16_f32 v34, v24, v25
	v_cvt_pkrtz_f16_f32 v35, v26, v27
	ds_write2_b64 v3, v[32:33], v[34:35] offset0:0 offset1:66
	v_pk_mul_f32 v[24:25], v[16:17], s[34:35] op_sel_hi:[1,0]
	v_pk_mul_f32 v[26:27], v[18:19], s[34:35] op_sel_hi:[1,0]
	v_pk_mul_f32 v[28:29], v[20:21], s[42:43] op_sel_hi:[1,0]
	v_pk_mul_f32 v[30:31], v[22:23], s[42:43] op_sel_hi:[1,0]
	v_mfma_f32_32x32x16_f16 v[72:87], v[184:187], v[12:15], v[72:87]
	v_cmp_lt_i32_e64 s[60:61], 0, v96
	v_cmp_lt_i32_e64 s[62:63], 0, v97
	v_cmp_lt_i32_e64 s[64:65], 0, v98
	v_cmp_lt_i32_e64 s[66:67], 0, v99
	v_max_f32_e32 v24, v24, v28
	v_max_f32_e32 v25, v25, v29
	v_max_f32_e32 v26, v26, v30
	v_max_f32_e32 v27, v27, v31
	v_cndmask_b32_e64 v24, 0, v24, s[60:61]
	v_cndmask_b32_e64 v25, 0, v25, s[62:63]
	v_cndmask_b32_e64 v26, 0, v26, s[64:65]
	v_cndmask_b32_e64 v27, 0, v27, s[66:67]
	v_mfma_f32_32x32x16_f16 v[40:55], v[188:191], v[208:211], v[40:55]
	v_cvt_pkrtz_f16_f32 v32, v24, v25
	v_cvt_pkrtz_f16_f32 v33, v26, v27
	v_pk_mul_f32 v[24:25], v[16:17], s[34:35] op_sel:[0,1] op_sel_hi:[1,1]
	v_pk_mul_f32 v[26:27], v[18:19], s[34:35] op_sel:[0,1] op_sel_hi:[1,1]
	v_pk_mul_f32 v[28:29], v[20:21], s[42:43] op_sel:[0,1] op_sel_hi:[1,1]
	v_pk_mul_f32 v[30:31], v[22:23], s[42:43] op_sel:[0,1] op_sel_hi:[1,1]
	v_mfma_f32_32x32x16_f16 v[56:71], v[188:191], v[212:215], v[56:71]
	v_cmp_lt_i32_e64 s[60:61], 0, v100
	v_cmp_lt_i32_e64 s[62:63], 0, v101
	v_cmp_lt_i32_e64 s[64:65], 0, v102
	v_cmp_lt_i32_e64 s[66:67], 0, v103
	v_max_f32_e32 v24, v24, v28
	v_max_f32_e32 v25, v25, v29
	v_max_f32_e32 v26, v26, v30
	v_max_f32_e32 v27, v27, v31
	v_cndmask_b32_e64 v24, 0, v24, s[60:61]
	v_cndmask_b32_e64 v25, 0, v25, s[62:63]
	v_cndmask_b32_e64 v26, 0, v26, s[64:65]
	v_cndmask_b32_e64 v27, 0, v27, s[66:67]
	v_mfma_f32_32x32x16_f16 v[72:87], v[188:191], v[12:15], v[72:87]
	v_cvt_pkrtz_f16_f32 v34, v24, v25
	v_cvt_pkrtz_f16_f32 v35, v26, v27
	ds_write2_b64 v3, v[32:33], v[34:35] offset0:132 offset1:198
	v_pk_mul_f32 v[24:25], v[16:17], s[36:37] op_sel_hi:[1,0]
	v_pk_mul_f32 v[26:27], v[18:19], s[36:37] op_sel_hi:[1,0]
	v_pk_mul_f32 v[28:29], v[20:21], s[44:45] op_sel_hi:[1,0]
	v_pk_mul_f32 v[30:31], v[22:23], s[44:45] op_sel_hi:[1,0]
	v_mfma_f32_32x32x16_f16 v[40:55], v[192:195], v[216:219], v[40:55]
	v_cmp_lt_i32_e64 s[60:61], 0, v104
	v_cmp_lt_i32_e64 s[62:63], 0, v105
	v_cmp_lt_i32_e64 s[64:65], 0, v106
	v_cmp_lt_i32_e64 s[66:67], 0, v107
	v_max_f32_e32 v24, v24, v28
	v_max_f32_e32 v25, v25, v29
	v_max_f32_e32 v26, v26, v30
	v_max_f32_e32 v27, v27, v31
	v_cndmask_b32_e64 v24, 0, v24, s[60:61]
	v_cndmask_b32_e64 v25, 0, v25, s[62:63]
	v_cndmask_b32_e64 v26, 0, v26, s[64:65]
	v_cndmask_b32_e64 v27, 0, v27, s[66:67]
	v_mfma_f32_32x32x16_f16 v[56:71], v[192:195], v[220:223], v[56:71]
	v_cvt_pkrtz_f16_f32 v32, v24, v25
	v_cvt_pkrtz_f16_f32 v33, v26, v27
	v_pk_mul_f32 v[24:25], v[16:17], s[36:37] op_sel:[0,1] op_sel_hi:[1,1]
	v_pk_mul_f32 v[26:27], v[18:19], s[36:37] op_sel:[0,1] op_sel_hi:[1,1]
	v_pk_mul_f32 v[28:29], v[20:21], s[44:45] op_sel:[0,1] op_sel_hi:[1,1]
	v_pk_mul_f32 v[30:31], v[22:23], s[44:45] op_sel:[0,1] op_sel_hi:[1,1]
	v_mfma_f32_32x32x16_f16 v[72:87], v[192:195], v[12:15], v[72:87]
	v_cmp_lt_i32_e64 s[60:61], 0, v108
	v_cmp_lt_i32_e64 s[62:63], 0, v109
	v_cmp_lt_i32_e64 s[64:65], 0, v110
	v_cmp_lt_i32_e64 s[66:67], 0, v111
	v_max_f32_e32 v24, v24, v28
	v_max_f32_e32 v25, v25, v29
	v_max_f32_e32 v26, v26, v30
	v_max_f32_e32 v27, v27, v31
	v_cndmask_b32_e64 v24, 0, v24, s[60:61]
	v_cndmask_b32_e64 v25, 0, v25, s[62:63]
	v_cndmask_b32_e64 v26, 0, v26, s[64:65]
	v_cndmask_b32_e64 v27, 0, v27, s[66:67]
	v_mfma_f32_32x32x16_f16 v[40:55], v[196:199], v[224:227], v[40:55]
	v_cvt_pkrtz_f16_f32 v34, v24, v25
	v_cvt_pkrtz_f16_f32 v35, v26, v27
	ds_write2_b64 v4, v[32:33], v[34:35] offset0:0 offset1:66
	v_pk_mul_f32 v[24:25], v[16:17], s[38:39] op_sel_hi:[1,0]
	v_pk_mul_f32 v[26:27], v[18:19], s[38:39] op_sel_hi:[1,0]
	v_pk_mul_f32 v[28:29], v[20:21], s[46:47] op_sel_hi:[1,0]
	v_pk_mul_f32 v[30:31], v[22:23], s[46:47] op_sel_hi:[1,0]
	v_mfma_f32_32x32x16_f16 v[56:71], v[196:199], v[228:231], v[56:71]
	v_cmp_lt_i32_e64 s[60:61], 0, v112
	v_cmp_lt_i32_e64 s[62:63], 0, v113
	v_cmp_lt_i32_e64 s[64:65], 0, v114
	v_cmp_lt_i32_e64 s[66:67], 0, v115
	v_max_f32_e32 v24, v24, v28
	v_max_f32_e32 v25, v25, v29
	v_max_f32_e32 v26, v26, v30
	v_max_f32_e32 v27, v27, v31
	v_cndmask_b32_e64 v24, 0, v24, s[60:61]
	v_cndmask_b32_e64 v25, 0, v25, s[62:63]
	v_cndmask_b32_e64 v26, 0, v26, s[64:65]
	v_cndmask_b32_e64 v27, 0, v27, s[66:67]
	v_cvt_pkrtz_f16_f32 v32, v24, v25
	v_cvt_pkrtz_f16_f32 v33, v26, v27
	v_pk_mul_f32 v[24:25], v[16:17], s[38:39] op_sel:[0,1] op_sel_hi:[1,1]
	v_pk_mul_f32 v[26:27], v[18:19], s[38:39] op_sel:[0,1] op_sel_hi:[1,1]
	v_pk_mul_f32 v[28:29], v[20:21], s[46:47] op_sel:[0,1] op_sel_hi:[1,1]
	v_pk_mul_f32 v[30:31], v[22:23], s[46:47] op_sel:[0,1] op_sel_hi:[1,1]
	v_mfma_f32_32x32x16_f16 v[72:87], v[196:199], v[12:15], v[72:87]
	v_cmp_lt_i32_e64 s[60:61], 0, v116
	v_cmp_lt_i32_e64 s[62:63], 0, v117
	v_cmp_lt_i32_e64 s[64:65], 0, v118
	v_cmp_lt_i32_e64 s[66:67], 0, v119
	v_max_f32_e32 v24, v24, v28
	v_max_f32_e32 v25, v25, v29
	v_max_f32_e32 v26, v26, v30
	v_max_f32_e32 v27, v27, v31
	v_cndmask_b32_e64 v24, 0, v24, s[60:61]
	v_cndmask_b32_e64 v25, 0, v25, s[62:63]
	v_cndmask_b32_e64 v26, 0, v26, s[64:65]
	v_cndmask_b32_e64 v27, 0, v27, s[66:67]
	v_cvt_pkrtz_f16_f32 v34, v24, v25
	v_cvt_pkrtz_f16_f32 v35, v26, v27
	ds_write2_b64 v4, v[32:33], v[34:35] offset0:132 offset1:198
	ds_write_b128 v9, v[152:155] offset:0
	ds_write_b128 v9, v[156:159] offset:1024
	ds_write_b128 v9, v[160:163] offset:2048
	ds_write_b128 v9, v[164:167] offset:3072
	s_add_u32 s3, s19, 3
	s_and_b32 s3, s3, 7
	s_lshl_b32 s3, s3, 10
	v_add_u32_e32 v11, s3, v10
	ds_read_b128 v[16:19], v11
	ds_read_b128 v[20:23], v11 offset:8192
	s_waitcnt lgkmcnt(0)
	s_barrier
	ds_read_b128 v[184:187], v7 offset:0
	ds_read_b128 v[200:203], v8 offset:0
	ds_read_b128 v[204:207], v8 offset:1024
	ds_read_b128 v[188:191], v7 offset:32
	ds_read_b128 v[208:211], v8 offset:2048
	ds_read_b128 v[212:215], v8 offset:3072
	ds_read_b128 v[192:195], v7 offset:64
	ds_read_b128 v[216:219], v8 offset:4096
	ds_read_b128 v[220:223], v8 offset:5120
	ds_read_b128 v[196:199], v7 offset:96
	ds_read_b128 v[224:227], v8 offset:6144
	ds_read_b128 v[228:231], v8 offset:7168
	s_add_u32 s3, s19, 4
	s_and_b32 s3, s3, 7
	s_lshl_b32 s57, s3, 10
	s_add_u32 s48, s57, s22
	s_add_u32 s49, s48, 0x2000
	s_add_u32 s50, s48, 0x4000
	s_add_u32 s51, s48, 0x6000
	s_add_u32 s52, s48, 0x8000
	s_add_u32 s53, s48, 0xa000
	s_add_u32 s54, s48, 0xc000
	s_add_u32 s55, s48, 0xe000
	s_lshl_b32 s56, s3, 15
	s_add_u32 s56, s56, s23
	buffer_load_dwordx4 v[88:91], v1, s[4:7], s48 offen nt
	buffer_load_dwordx4 v[92:95], v1, s[4:7], s49 offen nt
	buffer_load_dwordx4 v[96:99], v1, s[4:7], s50 offen nt
	buffer_load_dwordx4 v[100:103], v1, s[4:7], s51 offen nt
	buffer_load_dwordx4 v[104:107], v1, s[4:7], s52 offen nt
	buffer_load_dwordx4 v[108:111], v1, s[4:7], s53 offen nt
	buffer_load_dwordx4 v[112:115], v1, s[4:7], s54 offen nt
	buffer_load_dwordx4 v[116:119], v1, s[4:7], s55 offen nt
	buffer_load_dwordx4 v[152:155], v1, s[8:11], s56 offen
	buffer_load_dwordx4 v[156:159], v1, s[8:11], s56 offen offset:1024
	buffer_load_dwordx4 v[160:163], v1, s[8:11], s56 offen offset:2048
	buffer_load_dwordx4 v[164:167], v1, s[8:11], s56 offen offset:3072
	s_waitcnt vmcnt(12)
	v_pk_mul_f32 v[24:25], v[16:17], s[32:33] op_sel_hi:[1,0]
	v_pk_mul_f32 v[26:27], v[18:19], s[32:33] op_sel_hi:[1,0]
	v_pk_mul_f32 v[28:29], v[20:21], s[40:41] op_sel_hi:[1,0]
	v_pk_mul_f32 v[30:31], v[22:23], s[40:41] op_sel_hi:[1,0]
	v_cmp_lt_i32_e64 s[60:61], 0, v120
	v_cmp_lt_i32_e64 s[62:63], 0, v121
	v_cmp_lt_i32_e64 s[64:65], 0, v122
	v_cmp_lt_i32_e64 s[66:67], 0, v123
	v_max_f32_e32 v24, v24, v28
	v_max_f32_e32 v25, v25, v29
	v_max_f32_e32 v26, v26, v30
	v_max_f32_e32 v27, v27, v31
	v_cndmask_b32_e64 v24, 0, v24, s[60:61]
	v_cndmask_b32_e64 v25, 0, v25, s[62:63]
	v_cndmask_b32_e64 v26, 0, v26, s[64:65]
	v_cndmask_b32_e64 v27, 0, v27, s[66:67]
	v_cvt_pkrtz_f16_f32 v32, v24, v25
	v_cvt_pkrtz_f16_f32 v33, v26, v27
	s_waitcnt lgkmcnt(0)
	v_pk_mul_f32 v[24:25], v[16:17], s[32:33] op_sel:[0,1] op_sel_hi:[1,1]
	v_pk_mul_f32 v[26:27], v[18:19], s[32:33] op_sel:[0,1] op_sel_hi:[1,1]
	v_pk_mul_f32 v[28:29], v[20:21], s[40:41] op_sel:[0,1] op_sel_hi:[1,1]
	v_pk_mul_f32 v[30:31], v[22:23], s[40:41] op_sel:[0,1] op_sel_hi:[1,1]
	v_mfma_f32_32x32x16_f16 v[40:55], v[184:187], v[200:203], v[40:55]
	v_cmp_lt_i32_e64 s[60:61], 0, v124
	v_cmp_lt_i32_e64 s[62:63], 0, v125
	v_cmp_lt_i32_e64 s[64:65], 0, v126
	v_cmp_lt_i32_e64 s[66:67], 0, v127
	v_max_f32_e32 v24, v24, v28
	v_max_f32_e32 v25, v25, v29
	v_max_f32_e32 v26, v26, v30
	v_max_f32_e32 v27, v27, v31
	v_cndmask_b32_e64 v24, 0, v24, s[60:61]
	v_cndmask_b32_e64 v25, 0, v25, s[62:63]
	v_cndmask_b32_e64 v26, 0, v26, s[64:65]
	v_cndmask_b32_e64 v27, 0, v27, s[66:67]
	v_mfma_f32_32x32x16_f16 v[56:71], v[184:187], v[204:207], v[56:71]
	v_cvt_pkrtz_f16_f32 v34, v24, v25
	v_cvt_pkrtz_f16_f32 v35, v26, v27
	ds_write2_b64 v5, v[32:33], v[34:35] offset0:0 offset1:66
	v_pk_mul_f32 v[24:25], v[16:17], s[34:35] op_sel_hi:[1,0]
	v_pk_mul_f32 v[26:27], v[18:19], s[34:35] op_sel_hi:[1,0]
	v_pk_mul_f32 v[28:29], v[20:21], s[42:43] op_sel_hi:[1,0]
	v_pk_mul_f32 v[30:31], v[22:23], s[42:43] op_sel_hi:[1,0]
	v_mfma_f32_32x32x16_f16 v[72:87], v[184:187], v[12:15], v[72:87]
	v_cmp_lt_i32_e64 s[60:61], 0, v128
	v_cmp_lt_i32_e64 s[62:63], 0, v129
	v_cmp_lt_i32_e64 s[64:65], 0, v130
	v_cmp_lt_i32_e64 s[66:67], 0, v131
	v_max_f32_e32 v24, v24, v28
	v_max_f32_e32 v25, v25, v29
	v_max_f32_e32 v26, v26, v30
	v_max_f32_e32 v27, v27, v31
	v_cndmask_b32_e64 v24, 0, v24, s[60:61]
	v_cndmask_b32_e64 v25, 0, v25, s[62:63]
	v_cndmask_b32_e64 v26, 0, v26, s[64:65]
	v_cndmask_b32_e64 v27, 0, v27, s[66:67]
	v_mfma_f32_32x32x16_f16 v[40:55], v[188:191], v[208:211], v[40:55]
	v_cvt_pkrtz_f16_f32 v32, v24, v25
	v_cvt_pkrtz_f16_f32 v33, v26, v27
	v_pk_mul_f32 v[24:25], v[16:17], s[34:35] op_sel:[0,1] op_sel_hi:[1,1]
	v_pk_mul_f32 v[26:27], v[18:19], s[34:35] op_sel:[0,1] op_sel_hi:[1,1]
	v_pk_mul_f32 v[28:29], v[20:21], s[42:43] op_sel:[0,1] op_sel_hi:[1,1]
	v_pk_mul_f32 v[30:31], v[22:23], s[42:43] op_sel:[0,1] op_sel_hi:[1,1]
	v_mfma_f32_32x32x16_f16 v[56:71], v[188:191], v[212:215], v[56:71]
	v_cmp_lt_i32_e64 s[60:61], 0, v132
	v_cmp_lt_i32_e64 s[62:63], 0, v133
	v_cmp_lt_i32_e64 s[64:65], 0, v134
	v_cmp_lt_i32_e64 s[66:67], 0, v135
	v_max_f32_e32 v24, v24, v28
	v_max_f32_e32 v25, v25, v29
	v_max_f32_e32 v26, v26, v30
	v_max_f32_e32 v27, v27, v31
	v_cndmask_b32_e64 v24, 0, v24, s[60:61]
	v_cndmask_b32_e64 v25, 0, v25, s[62:63]
	v_cndmask_b32_e64 v26, 0, v26, s[64:65]
	v_cndmask_b32_e64 v27, 0, v27, s[66:67]
	v_mfma_f32_32x32x16_f16 v[72:87], v[188:191], v[12:15], v[72:87]
	v_cvt_pkrtz_f16_f32 v34, v24, v25
	v_cvt_pkrtz_f16_f32 v35, v26, v27
	ds_write2_b64 v5, v[32:33], v[34:35] offset0:132 offset1:198
	v_pk_mul_f32 v[24:25], v[16:17], s[36:37] op_sel_hi:[1,0]
	v_pk_mul_f32 v[26:27], v[18:19], s[36:37] op_sel_hi:[1,0]
	v_pk_mul_f32 v[28:29], v[20:21], s[44:45] op_sel_hi:[1,0]
	v_pk_mul_f32 v[30:31], v[22:23], s[44:45] op_sel_hi:[1,0]
	v_mfma_f32_32x32x16_f16 v[40:55], v[192:195], v[216:219], v[40:55]
	v_cmp_lt_i32_e64 s[60:61], 0, v136
	v_cmp_lt_i32_e64 s[62:63], 0, v137
	v_cmp_lt_i32_e64 s[64:65], 0, v138
	v_cmp_lt_i32_e64 s[66:67], 0, v139
	v_max_f32_e32 v24, v24, v28
	v_max_f32_e32 v25, v25, v29
	v_max_f32_e32 v26, v26, v30
	v_max_f32_e32 v27, v27, v31
	v_cndmask_b32_e64 v24, 0, v24, s[60:61]
	v_cndmask_b32_e64 v25, 0, v25, s[62:63]
	v_cndmask_b32_e64 v26, 0, v26, s[64:65]
	v_cndmask_b32_e64 v27, 0, v27, s[66:67]
	v_mfma_f32_32x32x16_f16 v[56:71], v[192:195], v[220:223], v[56:71]
	v_cvt_pkrtz_f16_f32 v32, v24, v25
	v_cvt_pkrtz_f16_f32 v33, v26, v27
	v_pk_mul_f32 v[24:25], v[16:17], s[36:37] op_sel:[0,1] op_sel_hi:[1,1]
	v_pk_mul_f32 v[26:27], v[18:19], s[36:37] op_sel:[0,1] op_sel_hi:[1,1]
	v_pk_mul_f32 v[28:29], v[20:21], s[44:45] op_sel:[0,1] op_sel_hi:[1,1]
	v_pk_mul_f32 v[30:31], v[22:23], s[44:45] op_sel:[0,1] op_sel_hi:[1,1]
	v_mfma_f32_32x32x16_f16 v[72:87], v[192:195], v[12:15], v[72:87]
	v_cmp_lt_i32_e64 s[60:61], 0, v140
	v_cmp_lt_i32_e64 s[62:63], 0, v141
	v_cmp_lt_i32_e64 s[64:65], 0, v142
	v_cmp_lt_i32_e64 s[66:67], 0, v143
	v_max_f32_e32 v24, v24, v28
	v_max_f32_e32 v25, v25, v29
	v_max_f32_e32 v26, v26, v30
	v_max_f32_e32 v27, v27, v31
	v_cndmask_b32_e64 v24, 0, v24, s[60:61]
	v_cndmask_b32_e64 v25, 0, v25, s[62:63]
	v_cndmask_b32_e64 v26, 0, v26, s[64:65]
	v_cndmask_b32_e64 v27, 0, v27, s[66:67]
	v_mfma_f32_32x32x16_f16 v[40:55], v[196:199], v[224:227], v[40:55]
	v_cvt_pkrtz_f16_f32 v34, v24, v25
	v_cvt_pkrtz_f16_f32 v35, v26, v27
	ds_write2_b64 v6, v[32:33], v[34:35] offset0:0 offset1:66
	v_pk_mul_f32 v[24:25], v[16:17], s[38:39] op_sel_hi:[1,0]
	v_pk_mul_f32 v[26:27], v[18:19], s[38:39] op_sel_hi:[1,0]
	v_pk_mul_f32 v[28:29], v[20:21], s[46:47] op_sel_hi:[1,0]
	v_pk_mul_f32 v[30:31], v[22:23], s[46:47] op_sel_hi:[1,0]
	v_mfma_f32_32x32x16_f16 v[56:71], v[196:199], v[228:231], v[56:71]
	v_cmp_lt_i32_e64 s[60:61], 0, v144
	v_cmp_lt_i32_e64 s[62:63], 0, v145
	v_cmp_lt_i32_e64 s[64:65], 0, v146
	v_cmp_lt_i32_e64 s[66:67], 0, v147
	v_max_f32_e32 v24, v24, v28
	v_max_f32_e32 v25, v25, v29
	v_max_f32_e32 v26, v26, v30
	v_max_f32_e32 v27, v27, v31
	v_cndmask_b32_e64 v24, 0, v24, s[60:61]
	v_cndmask_b32_e64 v25, 0, v25, s[62:63]
	v_cndmask_b32_e64 v26, 0, v26, s[64:65]
	v_cndmask_b32_e64 v27, 0, v27, s[66:67]
	v_cvt_pkrtz_f16_f32 v32, v24, v25
	v_cvt_pkrtz_f16_f32 v33, v26, v27
	v_pk_mul_f32 v[24:25], v[16:17], s[38:39] op_sel:[0,1] op_sel_hi:[1,1]
	v_pk_mul_f32 v[26:27], v[18:19], s[38:39] op_sel:[0,1] op_sel_hi:[1,1]
	v_pk_mul_f32 v[28:29], v[20:21], s[46:47] op_sel:[0,1] op_sel_hi:[1,1]
	v_pk_mul_f32 v[30:31], v[22:23], s[46:47] op_sel:[0,1] op_sel_hi:[1,1]
	v_mfma_f32_32x32x16_f16 v[72:87], v[196:199], v[12:15], v[72:87]
	v_cmp_lt_i32_e64 s[60:61], 0, v148
	v_cmp_lt_i32_e64 s[62:63], 0, v149
	v_cmp_lt_i32_e64 s[64:65], 0, v150
	v_cmp_lt_i32_e64 s[66:67], 0, v151
	v_max_f32_e32 v24, v24, v28
	v_max_f32_e32 v25, v25, v29
	v_max_f32_e32 v26, v26, v30
	v_max_f32_e32 v27, v27, v31
	v_cndmask_b32_e64 v24, 0, v24, s[60:61]
	v_cndmask_b32_e64 v25, 0, v25, s[62:63]
	v_cndmask_b32_e64 v26, 0, v26, s[64:65]
	v_cndmask_b32_e64 v27, 0, v27, s[66:67]
	v_cvt_pkrtz_f16_f32 v34, v24, v25
	v_cvt_pkrtz_f16_f32 v35, v26, v27
	ds_write2_b64 v6, v[32:33], v[34:35] offset0:132 offset1:198
	ds_write_b128 v9, v[168:171] offset:32768
	ds_write_b128 v9, v[172:175] offset:33792
	ds_write_b128 v9, v[176:179] offset:34816
	ds_write_b128 v9, v[180:183] offset:35840
	s_add_u32 s3, s19, 4
	s_and_b32 s3, s3, 7
	s_lshl_b32 s3, s3, 10
	v_add_u32_e32 v11, s3, v10
	ds_read_b128 v[16:19], v11
	ds_read_b128 v[20:23], v11 offset:8192
	s_waitcnt lgkmcnt(0)
	s_barrier
	ds_read_b128 v[184:187], v7 offset:33792
	ds_read_b128 v[200:203], v8 offset:32768
	ds_read_b128 v[204:207], v8 offset:33792
	ds_read_b128 v[188:191], v7 offset:33824
	ds_read_b128 v[208:211], v8 offset:34816
	ds_read_b128 v[212:215], v8 offset:35840
	ds_read_b128 v[192:195], v7 offset:33856
	ds_read_b128 v[216:219], v8 offset:36864
	ds_read_b128 v[220:223], v8 offset:37888
	ds_read_b128 v[196:199], v7 offset:33888
	ds_read_b128 v[224:227], v8 offset:38912
	ds_read_b128 v[228:231], v8 offset:39936
	s_add_u32 s3, s19, 5
	s_and_b32 s3, s3, 7
	s_lshl_b32 s57, s3, 10
	s_add_u32 s48, s57, s22
	s_add_u32 s49, s48, 0x2000
	s_add_u32 s50, s48, 0x4000
	s_add_u32 s51, s48, 0x6000
	s_add_u32 s52, s48, 0x8000
	s_add_u32 s53, s48, 0xa000
	s_add_u32 s54, s48, 0xc000
	s_add_u32 s55, s48, 0xe000
	s_lshl_b32 s56, s3, 15
	s_add_u32 s56, s56, s23
	buffer_load_dwordx4 v[120:123], v1, s[4:7], s48 offen nt
	buffer_load_dwordx4 v[124:127], v1, s[4:7], s49 offen nt
	buffer_load_dwordx4 v[128:131], v1, s[4:7], s50 offen nt
	buffer_load_dwordx4 v[132:135], v1, s[4:7], s51 offen nt
	buffer_load_dwordx4 v[136:139], v1, s[4:7], s52 offen nt
	buffer_load_dwordx4 v[140:143], v1, s[4:7], s53 offen nt
	buffer_load_dwordx4 v[144:147], v1, s[4:7], s54 offen nt
	buffer_load_dwordx4 v[148:151], v1, s[4:7], s55 offen nt
	buffer_load_dwordx4 v[168:171], v1, s[8:11], s56 offen
	buffer_load_dwordx4 v[172:175], v1, s[8:11], s56 offen offset:1024
	buffer_load_dwordx4 v[176:179], v1, s[8:11], s56 offen offset:2048
	buffer_load_dwordx4 v[180:183], v1, s[8:11], s56 offen offset:3072
	s_waitcnt vmcnt(12)
	v_pk_mul_f32 v[24:25], v[16:17], s[32:33] op_sel_hi:[1,0]
	v_pk_mul_f32 v[26:27], v[18:19], s[32:33] op_sel_hi:[1,0]
	v_pk_mul_f32 v[28:29], v[20:21], s[40:41] op_sel_hi:[1,0]
	v_pk_mul_f32 v[30:31], v[22:23], s[40:41] op_sel_hi:[1,0]
	v_cmp_lt_i32_e64 s[60:61], 0, v88
	v_cmp_lt_i32_e64 s[62:63], 0, v89
	v_cmp_lt_i32_e64 s[64:65], 0, v90
	v_cmp_lt_i32_e64 s[66:67], 0, v91
	v_max_f32_e32 v24, v24, v28
	v_max_f32_e32 v25, v25, v29
	v_max_f32_e32 v26, v26, v30
	v_max_f32_e32 v27, v27, v31
	v_cndmask_b32_e64 v24, 0, v24, s[60:61]
	v_cndmask_b32_e64 v25, 0, v25, s[62:63]
	v_cndmask_b32_e64 v26, 0, v26, s[64:65]
	v_cndmask_b32_e64 v27, 0, v27, s[66:67]
	v_cvt_pkrtz_f16_f32 v32, v24, v25
	v_cvt_pkrtz_f16_f32 v33, v26, v27
	s_waitcnt lgkmcnt(0)
	v_pk_mul_f32 v[24:25], v[16:17], s[32:33] op_sel:[0,1] op_sel_hi:[1,1]
	v_pk_mul_f32 v[26:27], v[18:19], s[32:33] op_sel:[0,1] op_sel_hi:[1,1]
	v_pk_mul_f32 v[28:29], v[20:21], s[40:41] op_sel:[0,1] op_sel_hi:[1,1]
	v_pk_mul_f32 v[30:31], v[22:23], s[40:41] op_sel:[0,1] op_sel_hi:[1,1]
	v_mfma_f32_32x32x16_f16 v[40:55], v[184:187], v[200:203], v[40:55]
	v_cmp_lt_i32_e64 s[60:61], 0, v92
	v_cmp_lt_i32_e64 s[62:63], 0, v93
	v_cmp_lt_i32_e64 s[64:65], 0, v94
	v_cmp_lt_i32_e64 s[66:67], 0, v95
	v_max_f32_e32 v24, v24, v28
	v_max_f32_e32 v25, v25, v29
	v_max_f32_e32 v26, v26, v30
	v_max_f32_e32 v27, v27, v31
	v_cndmask_b32_e64 v24, 0, v24, s[60:61]
	v_cndmask_b32_e64 v25, 0, v25, s[62:63]
	v_cndmask_b32_e64 v26, 0, v26, s[64:65]
	v_cndmask_b32_e64 v27, 0, v27, s[66:67]
	v_mfma_f32_32x32x16_f16 v[56:71], v[184:187], v[204:207], v[56:71]
	v_cvt_pkrtz_f16_f32 v34, v24, v25
	v_cvt_pkrtz_f16_f32 v35, v26, v27
	ds_write2_b64 v3, v[32:33], v[34:35] offset0:0 offset1:66
	v_pk_mul_f32 v[24:25], v[16:17], s[34:35] op_sel_hi:[1,0]
	v_pk_mul_f32 v[26:27], v[18:19], s[34:35] op_sel_hi:[1,0]
	v_pk_mul_f32 v[28:29], v[20:21], s[42:43] op_sel_hi:[1,0]
	v_pk_mul_f32 v[30:31], v[22:23], s[42:43] op_sel_hi:[1,0]
	v_mfma_f32_32x32x16_f16 v[72:87], v[184:187], v[12:15], v[72:87]
	v_cmp_lt_i32_e64 s[60:61], 0, v96
	v_cmp_lt_i32_e64 s[62:63], 0, v97
	v_cmp_lt_i32_e64 s[64:65], 0, v98
	v_cmp_lt_i32_e64 s[66:67], 0, v99
	v_max_f32_e32 v24, v24, v28
	v_max_f32_e32 v25, v25, v29
	v_max_f32_e32 v26, v26, v30
	v_max_f32_e32 v27, v27, v31
	v_cndmask_b32_e64 v24, 0, v24, s[60:61]
	v_cndmask_b32_e64 v25, 0, v25, s[62:63]
	v_cndmask_b32_e64 v26, 0, v26, s[64:65]
	v_cndmask_b32_e64 v27, 0, v27, s[66:67]
	v_mfma_f32_32x32x16_f16 v[40:55], v[188:191], v[208:211], v[40:55]
	v_cvt_pkrtz_f16_f32 v32, v24, v25
	v_cvt_pkrtz_f16_f32 v33, v26, v27
	v_pk_mul_f32 v[24:25], v[16:17], s[34:35] op_sel:[0,1] op_sel_hi:[1,1]
	v_pk_mul_f32 v[26:27], v[18:19], s[34:35] op_sel:[0,1] op_sel_hi:[1,1]
	v_pk_mul_f32 v[28:29], v[20:21], s[42:43] op_sel:[0,1] op_sel_hi:[1,1]
	v_pk_mul_f32 v[30:31], v[22:23], s[42:43] op_sel:[0,1] op_sel_hi:[1,1]
	v_mfma_f32_32x32x16_f16 v[56:71], v[188:191], v[212:215], v[56:71]
	v_cmp_lt_i32_e64 s[60:61], 0, v100
	v_cmp_lt_i32_e64 s[62:63], 0, v101
	v_cmp_lt_i32_e64 s[64:65], 0, v102
	v_cmp_lt_i32_e64 s[66:67], 0, v103
	v_max_f32_e32 v24, v24, v28
	v_max_f32_e32 v25, v25, v29
	v_max_f32_e32 v26, v26, v30
	v_max_f32_e32 v27, v27, v31
	v_cndmask_b32_e64 v24, 0, v24, s[60:61]
	v_cndmask_b32_e64 v25, 0, v25, s[62:63]
	v_cndmask_b32_e64 v26, 0, v26, s[64:65]
	v_cndmask_b32_e64 v27, 0, v27, s[66:67]
	v_mfma_f32_32x32x16_f16 v[72:87], v[188:191], v[12:15], v[72:87]
	v_cvt_pkrtz_f16_f32 v34, v24, v25
	v_cvt_pkrtz_f16_f32 v35, v26, v27
	ds_write2_b64 v3, v[32:33], v[34:35] offset0:132 offset1:198
	v_pk_mul_f32 v[24:25], v[16:17], s[36:37] op_sel_hi:[1,0]
	v_pk_mul_f32 v[26:27], v[18:19], s[36:37] op_sel_hi:[1,0]
	v_pk_mul_f32 v[28:29], v[20:21], s[44:45] op_sel_hi:[1,0]
	v_pk_mul_f32 v[30:31], v[22:23], s[44:45] op_sel_hi:[1,0]
	v_mfma_f32_32x32x16_f16 v[40:55], v[192:195], v[216:219], v[40:55]
	v_cmp_lt_i32_e64 s[60:61], 0, v104
	v_cmp_lt_i32_e64 s[62:63], 0, v105
	v_cmp_lt_i32_e64 s[64:65], 0, v106
	v_cmp_lt_i32_e64 s[66:67], 0, v107
	v_max_f32_e32 v24, v24, v28
	v_max_f32_e32 v25, v25, v29
	v_max_f32_e32 v26, v26, v30
	v_max_f32_e32 v27, v27, v31
	v_cndmask_b32_e64 v24, 0, v24, s[60:61]
	v_cndmask_b32_e64 v25, 0, v25, s[62:63]
	v_cndmask_b32_e64 v26, 0, v26, s[64:65]
	v_cndmask_b32_e64 v27, 0, v27, s[66:67]
	v_mfma_f32_32x32x16_f16 v[56:71], v[192:195], v[220:223], v[56:71]
	v_cvt_pkrtz_f16_f32 v32, v24, v25
	v_cvt_pkrtz_f16_f32 v33, v26, v27
	v_pk_mul_f32 v[24:25], v[16:17], s[36:37] op_sel:[0,1] op_sel_hi:[1,1]
	v_pk_mul_f32 v[26:27], v[18:19], s[36:37] op_sel:[0,1] op_sel_hi:[1,1]
	v_pk_mul_f32 v[28:29], v[20:21], s[44:45] op_sel:[0,1] op_sel_hi:[1,1]
	v_pk_mul_f32 v[30:31], v[22:23], s[44:45] op_sel:[0,1] op_sel_hi:[1,1]
	v_mfma_f32_32x32x16_f16 v[72:87], v[192:195], v[12:15], v[72:87]
	v_cmp_lt_i32_e64 s[60:61], 0, v108
	v_cmp_lt_i32_e64 s[62:63], 0, v109
	v_cmp_lt_i32_e64 s[64:65], 0, v110
	v_cmp_lt_i32_e64 s[66:67], 0, v111
	v_max_f32_e32 v24, v24, v28
	v_max_f32_e32 v25, v25, v29
	v_max_f32_e32 v26, v26, v30
	v_max_f32_e32 v27, v27, v31
	v_cndmask_b32_e64 v24, 0, v24, s[60:61]
	v_cndmask_b32_e64 v25, 0, v25, s[62:63]
	v_cndmask_b32_e64 v26, 0, v26, s[64:65]
	v_cndmask_b32_e64 v27, 0, v27, s[66:67]
	v_mfma_f32_32x32x16_f16 v[40:55], v[196:199], v[224:227], v[40:55]
	v_cvt_pkrtz_f16_f32 v34, v24, v25
	v_cvt_pkrtz_f16_f32 v35, v26, v27
	ds_write2_b64 v4, v[32:33], v[34:35] offset0:0 offset1:66
	v_pk_mul_f32 v[24:25], v[16:17], s[38:39] op_sel_hi:[1,0]
	v_pk_mul_f32 v[26:27], v[18:19], s[38:39] op_sel_hi:[1,0]
	v_pk_mul_f32 v[28:29], v[20:21], s[46:47] op_sel_hi:[1,0]
	v_pk_mul_f32 v[30:31], v[22:23], s[46:47] op_sel_hi:[1,0]
	v_mfma_f32_32x32x16_f16 v[56:71], v[196:199], v[228:231], v[56:71]
	v_cmp_lt_i32_e64 s[60:61], 0, v112
	v_cmp_lt_i32_e64 s[62:63], 0, v113
	v_cmp_lt_i32_e64 s[64:65], 0, v114
	v_cmp_lt_i32_e64 s[66:67], 0, v115
	v_max_f32_e32 v24, v24, v28
	v_max_f32_e32 v25, v25, v29
	v_max_f32_e32 v26, v26, v30
	v_max_f32_e32 v27, v27, v31
	v_cndmask_b32_e64 v24, 0, v24, s[60:61]
	v_cndmask_b32_e64 v25, 0, v25, s[62:63]
	v_cndmask_b32_e64 v26, 0, v26, s[64:65]
	v_cndmask_b32_e64 v27, 0, v27, s[66:67]
	v_cvt_pkrtz_f16_f32 v32, v24, v25
	v_cvt_pkrtz_f16_f32 v33, v26, v27
	v_pk_mul_f32 v[24:25], v[16:17], s[38:39] op_sel:[0,1] op_sel_hi:[1,1]
	v_pk_mul_f32 v[26:27], v[18:19], s[38:39] op_sel:[0,1] op_sel_hi:[1,1]
	v_pk_mul_f32 v[28:29], v[20:21], s[46:47] op_sel:[0,1] op_sel_hi:[1,1]
	v_pk_mul_f32 v[30:31], v[22:23], s[46:47] op_sel:[0,1] op_sel_hi:[1,1]
	v_mfma_f32_32x32x16_f16 v[72:87], v[196:199], v[12:15], v[72:87]
	v_cmp_lt_i32_e64 s[60:61], 0, v116
	v_cmp_lt_i32_e64 s[62:63], 0, v117
	v_cmp_lt_i32_e64 s[64:65], 0, v118
	v_cmp_lt_i32_e64 s[66:67], 0, v119
	v_max_f32_e32 v24, v24, v28
	v_max_f32_e32 v25, v25, v29
	v_max_f32_e32 v26, v26, v30
	v_max_f32_e32 v27, v27, v31
	v_cndmask_b32_e64 v24, 0, v24, s[60:61]
	v_cndmask_b32_e64 v25, 0, v25, s[62:63]
	v_cndmask_b32_e64 v26, 0, v26, s[64:65]
	v_cndmask_b32_e64 v27, 0, v27, s[66:67]
	v_cvt_pkrtz_f16_f32 v34, v24, v25
	v_cvt_pkrtz_f16_f32 v35, v26, v27
	ds_write2_b64 v4, v[32:33], v[34:35] offset0:132 offset1:198
	ds_write_b128 v9, v[152:155] offset:0
	ds_write_b128 v9, v[156:159] offset:1024
	ds_write_b128 v9, v[160:163] offset:2048
	ds_write_b128 v9, v[164:167] offset:3072
	s_add_u32 s3, s19, 5
	s_and_b32 s3, s3, 7
	s_lshl_b32 s3, s3, 10
	v_add_u32_e32 v11, s3, v10
	ds_read_b128 v[16:19], v11
	ds_read_b128 v[20:23], v11 offset:8192
	s_waitcnt lgkmcnt(0)
	s_barrier
	ds_read_b128 v[184:187], v7 offset:0
	ds_read_b128 v[200:203], v8 offset:0
	ds_read_b128 v[204:207], v8 offset:1024
	ds_read_b128 v[188:191], v7 offset:32
	ds_read_b128 v[208:211], v8 offset:2048
	ds_read_b128 v[212:215], v8 offset:3072
	ds_read_b128 v[192:195], v7 offset:64
	ds_read_b128 v[216:219], v8 offset:4096
	ds_read_b128 v[220:223], v8 offset:5120
	ds_read_b128 v[196:199], v7 offset:96
	ds_read_b128 v[224:227], v8 offset:6144
	ds_read_b128 v[228:231], v8 offset:7168
	s_add_u32 s3, s19, 6
	s_and_b32 s3, s3, 7
	s_lshl_b32 s57, s3, 10
	s_add_u32 s48, s57, s22
	s_add_u32 s49, s48, 0x2000
	s_add_u32 s50, s48, 0x4000
	s_add_u32 s51, s48, 0x6000
	s_add_u32 s52, s48, 0x8000
	s_add_u32 s53, s48, 0xa000
	s_add_u32 s54, s48, 0xc000
	s_add_u32 s55, s48, 0xe000
	s_lshl_b32 s56, s3, 15
	s_add_u32 s56, s56, s23
	buffer_load_dwordx4 v[88:91], v1, s[4:7], s48 offen nt
	buffer_load_dwordx4 v[92:95], v1, s[4:7], s49 offen nt
	buffer_load_dwordx4 v[96:99], v1, s[4:7], s50 offen nt
	buffer_load_dwordx4 v[100:103], v1, s[4:7], s51 offen nt
	buffer_load_dwordx4 v[104:107], v1, s[4:7], s52 offen nt
	buffer_load_dwordx4 v[108:111], v1, s[4:7], s53 offen nt
	buffer_load_dwordx4 v[112:115], v1, s[4:7], s54 offen nt
	buffer_load_dwordx4 v[116:119], v1, s[4:7], s55 offen nt
	buffer_load_dwordx4 v[152:155], v1, s[8:11], s56 offen
	buffer_load_dwordx4 v[156:159], v1, s[8:11], s56 offen offset:1024
	buffer_load_dwordx4 v[160:163], v1, s[8:11], s56 offen offset:2048
	buffer_load_dwordx4 v[164:167], v1, s[8:11], s56 offen offset:3072
	s_waitcnt vmcnt(12)
	v_pk_mul_f32 v[24:25], v[16:17], s[32:33] op_sel_hi:[1,0]
	v_pk_mul_f32 v[26:27], v[18:19], s[32:33] op_sel_hi:[1,0]
	v_pk_mul_f32 v[28:29], v[20:21], s[40:41] op_sel_hi:[1,0]
	v_pk_mul_f32 v[30:31], v[22:23], s[40:41] op_sel_hi:[1,0]
	v_cmp_lt_i32_e64 s[60:61], 0, v120
	v_cmp_lt_i32_e64 s[62:63], 0, v121
	v_cmp_lt_i32_e64 s[64:65], 0, v122
	v_cmp_lt_i32_e64 s[66:67], 0, v123
	v_max_f32_e32 v24, v24, v28
	v_max_f32_e32 v25, v25, v29
	v_max_f32_e32 v26, v26, v30
	v_max_f32_e32 v27, v27, v31
	v_cndmask_b32_e64 v24, 0, v24, s[60:61]
	v_cndmask_b32_e64 v25, 0, v25, s[62:63]
	v_cndmask_b32_e64 v26, 0, v26, s[64:65]
	v_cndmask_b32_e64 v27, 0, v27, s[66:67]
	v_cvt_pkrtz_f16_f32 v32, v24, v25
	v_cvt_pkrtz_f16_f32 v33, v26, v27
	s_waitcnt lgkmcnt(0)
	v_pk_mul_f32 v[24:25], v[16:17], s[32:33] op_sel:[0,1] op_sel_hi:[1,1]
	v_pk_mul_f32 v[26:27], v[18:19], s[32:33] op_sel:[0,1] op_sel_hi:[1,1]
	v_pk_mul_f32 v[28:29], v[20:21], s[40:41] op_sel:[0,1] op_sel_hi:[1,1]
	v_pk_mul_f32 v[30:31], v[22:23], s[40:41] op_sel:[0,1] op_sel_hi:[1,1]
	v_mfma_f32_32x32x16_f16 v[40:55], v[184:187], v[200:203], v[40:55]
	v_cmp_lt_i32_e64 s[60:61], 0, v124
	v_cmp_lt_i32_e64 s[62:63], 0, v125
	v_cmp_lt_i32_e64 s[64:65], 0, v126
	v_cmp_lt_i32_e64 s[66:67], 0, v127
	v_max_f32_e32 v24, v24, v28
	v_max_f32_e32 v25, v25, v29
	v_max_f32_e32 v26, v26, v30
	v_max_f32_e32 v27, v27, v31
	v_cndmask_b32_e64 v24, 0, v24, s[60:61]
	v_cndmask_b32_e64 v25, 0, v25, s[62:63]
	v_cndmask_b32_e64 v26, 0, v26, s[64:65]
	v_cndmask_b32_e64 v27, 0, v27, s[66:67]
	v_mfma_f32_32x32x16_f16 v[56:71], v[184:187], v[204:207], v[56:71]
	v_cvt_pkrtz_f16_f32 v34, v24, v25
	v_cvt_pkrtz_f16_f32 v35, v26, v27
	ds_write2_b64 v5, v[32:33], v[34:35] offset0:0 offset1:66
	v_pk_mul_f32 v[24:25], v[16:17], s[34:35] op_sel_hi:[1,0]
	v_pk_mul_f32 v[26:27], v[18:19], s[34:35] op_sel_hi:[1,0]
	v_pk_mul_f32 v[28:29], v[20:21], s[42:43] op_sel_hi:[1,0]
	v_pk_mul_f32 v[30:31], v[22:23], s[42:43] op_sel_hi:[1,0]
	v_mfma_f32_32x32x16_f16 v[72:87], v[184:187], v[12:15], v[72:87]
	v_cmp_lt_i32_e64 s[60:61], 0, v128
	v_cmp_lt_i32_e64 s[62:63], 0, v129
	v_cmp_lt_i32_e64 s[64:65], 0, v130
	v_cmp_lt_i32_e64 s[66:67], 0, v131
	v_max_f32_e32 v24, v24, v28
	v_max_f32_e32 v25, v25, v29
	v_max_f32_e32 v26, v26, v30
	v_max_f32_e32 v27, v27, v31
	v_cndmask_b32_e64 v24, 0, v24, s[60:61]
	v_cndmask_b32_e64 v25, 0, v25, s[62:63]
	v_cndmask_b32_e64 v26, 0, v26, s[64:65]
	v_cndmask_b32_e64 v27, 0, v27, s[66:67]
	v_mfma_f32_32x32x16_f16 v[40:55], v[188:191], v[208:211], v[40:55]
	v_cvt_pkrtz_f16_f32 v32, v24, v25
	v_cvt_pkrtz_f16_f32 v33, v26, v27
	v_pk_mul_f32 v[24:25], v[16:17], s[34:35] op_sel:[0,1] op_sel_hi:[1,1]
	v_pk_mul_f32 v[26:27], v[18:19], s[34:35] op_sel:[0,1] op_sel_hi:[1,1]
	v_pk_mul_f32 v[28:29], v[20:21], s[42:43] op_sel:[0,1] op_sel_hi:[1,1]
	v_pk_mul_f32 v[30:31], v[22:23], s[42:43] op_sel:[0,1] op_sel_hi:[1,1]
	v_mfma_f32_32x32x16_f16 v[56:71], v[188:191], v[212:215], v[56:71]
	v_cmp_lt_i32_e64 s[60:61], 0, v132
	v_cmp_lt_i32_e64 s[62:63], 0, v133
	v_cmp_lt_i32_e64 s[64:65], 0, v134
	v_cmp_lt_i32_e64 s[66:67], 0, v135
	v_max_f32_e32 v24, v24, v28
	v_max_f32_e32 v25, v25, v29
	v_max_f32_e32 v26, v26, v30
	v_max_f32_e32 v27, v27, v31
	v_cndmask_b32_e64 v24, 0, v24, s[60:61]
	v_cndmask_b32_e64 v25, 0, v25, s[62:63]
	v_cndmask_b32_e64 v26, 0, v26, s[64:65]
	v_cndmask_b32_e64 v27, 0, v27, s[66:67]
	v_mfma_f32_32x32x16_f16 v[72:87], v[188:191], v[12:15], v[72:87]
	v_cvt_pkrtz_f16_f32 v34, v24, v25
	v_cvt_pkrtz_f16_f32 v35, v26, v27
	ds_write2_b64 v5, v[32:33], v[34:35] offset0:132 offset1:198
	v_pk_mul_f32 v[24:25], v[16:17], s[36:37] op_sel_hi:[1,0]
	v_pk_mul_f32 v[26:27], v[18:19], s[36:37] op_sel_hi:[1,0]
	v_pk_mul_f32 v[28:29], v[20:21], s[44:45] op_sel_hi:[1,0]
	v_pk_mul_f32 v[30:31], v[22:23], s[44:45] op_sel_hi:[1,0]
	v_mfma_f32_32x32x16_f16 v[40:55], v[192:195], v[216:219], v[40:55]
	v_cmp_lt_i32_e64 s[60:61], 0, v136
	v_cmp_lt_i32_e64 s[62:63], 0, v137
	v_cmp_lt_i32_e64 s[64:65], 0, v138
	v_cmp_lt_i32_e64 s[66:67], 0, v139
	v_max_f32_e32 v24, v24, v28
	v_max_f32_e32 v25, v25, v29
	v_max_f32_e32 v26, v26, v30
	v_max_f32_e32 v27, v27, v31
	v_cndmask_b32_e64 v24, 0, v24, s[60:61]
	v_cndmask_b32_e64 v25, 0, v25, s[62:63]
	v_cndmask_b32_e64 v26, 0, v26, s[64:65]
	v_cndmask_b32_e64 v27, 0, v27, s[66:67]
	v_mfma_f32_32x32x16_f16 v[56:71], v[192:195], v[220:223], v[56:71]
	v_cvt_pkrtz_f16_f32 v32, v24, v25
	v_cvt_pkrtz_f16_f32 v33, v26, v27
	v_pk_mul_f32 v[24:25], v[16:17], s[36:37] op_sel:[0,1] op_sel_hi:[1,1]
	v_pk_mul_f32 v[26:27], v[18:19], s[36:37] op_sel:[0,1] op_sel_hi:[1,1]
	v_pk_mul_f32 v[28:29], v[20:21], s[44:45] op_sel:[0,1] op_sel_hi:[1,1]
	v_pk_mul_f32 v[30:31], v[22:23], s[44:45] op_sel:[0,1] op_sel_hi:[1,1]
	v_mfma_f32_32x32x16_f16 v[72:87], v[192:195], v[12:15], v[72:87]
	v_cmp_lt_i32_e64 s[60:61], 0, v140
	v_cmp_lt_i32_e64 s[62:63], 0, v141
	v_cmp_lt_i32_e64 s[64:65], 0, v142
	v_cmp_lt_i32_e64 s[66:67], 0, v143
	v_max_f32_e32 v24, v24, v28
	v_max_f32_e32 v25, v25, v29
	v_max_f32_e32 v26, v26, v30
	v_max_f32_e32 v27, v27, v31
	v_cndmask_b32_e64 v24, 0, v24, s[60:61]
	v_cndmask_b32_e64 v25, 0, v25, s[62:63]
	v_cndmask_b32_e64 v26, 0, v26, s[64:65]
	v_cndmask_b32_e64 v27, 0, v27, s[66:67]
	v_mfma_f32_32x32x16_f16 v[40:55], v[196:199], v[224:227], v[40:55]
	v_cvt_pkrtz_f16_f32 v34, v24, v25
	v_cvt_pkrtz_f16_f32 v35, v26, v27
	ds_write2_b64 v6, v[32:33], v[34:35] offset0:0 offset1:66
	v_pk_mul_f32 v[24:25], v[16:17], s[38:39] op_sel_hi:[1,0]
	v_pk_mul_f32 v[26:27], v[18:19], s[38:39] op_sel_hi:[1,0]
	v_pk_mul_f32 v[28:29], v[20:21], s[46:47] op_sel_hi:[1,0]
	v_pk_mul_f32 v[30:31], v[22:23], s[46:47] op_sel_hi:[1,0]
	v_mfma_f32_32x32x16_f16 v[56:71], v[196:199], v[228:231], v[56:71]
	v_cmp_lt_i32_e64 s[60:61], 0, v144
	v_cmp_lt_i32_e64 s[62:63], 0, v145
	v_cmp_lt_i32_e64 s[64:65], 0, v146
	v_cmp_lt_i32_e64 s[66:67], 0, v147
	v_max_f32_e32 v24, v24, v28
	v_max_f32_e32 v25, v25, v29
	v_max_f32_e32 v26, v26, v30
	v_max_f32_e32 v27, v27, v31
	v_cndmask_b32_e64 v24, 0, v24, s[60:61]
	v_cndmask_b32_e64 v25, 0, v25, s[62:63]
	v_cndmask_b32_e64 v26, 0, v26, s[64:65]
	v_cndmask_b32_e64 v27, 0, v27, s[66:67]
	v_cvt_pkrtz_f16_f32 v32, v24, v25
	v_cvt_pkrtz_f16_f32 v33, v26, v27
	v_pk_mul_f32 v[24:25], v[16:17], s[38:39] op_sel:[0,1] op_sel_hi:[1,1]
	v_pk_mul_f32 v[26:27], v[18:19], s[38:39] op_sel:[0,1] op_sel_hi:[1,1]
	v_pk_mul_f32 v[28:29], v[20:21], s[46:47] op_sel:[0,1] op_sel_hi:[1,1]
	v_pk_mul_f32 v[30:31], v[22:23], s[46:47] op_sel:[0,1] op_sel_hi:[1,1]
	v_mfma_f32_32x32x16_f16 v[72:87], v[196:199], v[12:15], v[72:87]
	v_cmp_lt_i32_e64 s[60:61], 0, v148
	v_cmp_lt_i32_e64 s[62:63], 0, v149
	v_cmp_lt_i32_e64 s[64:65], 0, v150
	v_cmp_lt_i32_e64 s[66:67], 0, v151
	v_max_f32_e32 v24, v24, v28
	v_max_f32_e32 v25, v25, v29
	v_max_f32_e32 v26, v26, v30
	v_max_f32_e32 v27, v27, v31
	v_cndmask_b32_e64 v24, 0, v24, s[60:61]
	v_cndmask_b32_e64 v25, 0, v25, s[62:63]
	v_cndmask_b32_e64 v26, 0, v26, s[64:65]
	v_cndmask_b32_e64 v27, 0, v27, s[66:67]
	v_cvt_pkrtz_f16_f32 v34, v24, v25
	v_cvt_pkrtz_f16_f32 v35, v26, v27
	ds_write2_b64 v6, v[32:33], v[34:35] offset0:132 offset1:198
	ds_write_b128 v9, v[168:171] offset:32768
	ds_write_b128 v9, v[172:175] offset:33792
	ds_write_b128 v9, v[176:179] offset:34816
	ds_write_b128 v9, v[180:183] offset:35840
	s_add_u32 s3, s19, 6
	s_and_b32 s3, s3, 7
	s_lshl_b32 s3, s3, 10
	v_add_u32_e32 v11, s3, v10
	ds_read_b128 v[16:19], v11
	ds_read_b128 v[20:23], v11 offset:8192
	s_waitcnt lgkmcnt(0)
	s_barrier
	ds_read_b128 v[184:187], v7 offset:33792
	ds_read_b128 v[200:203], v8 offset:32768
	ds_read_b128 v[204:207], v8 offset:33792
	ds_read_b128 v[188:191], v7 offset:33824
	ds_read_b128 v[208:211], v8 offset:34816
	ds_read_b128 v[212:215], v8 offset:35840
	ds_read_b128 v[192:195], v7 offset:33856
	ds_read_b128 v[216:219], v8 offset:36864
	ds_read_b128 v[220:223], v8 offset:37888
	ds_read_b128 v[196:199], v7 offset:33888
	ds_read_b128 v[224:227], v8 offset:38912
	ds_read_b128 v[228:231], v8 offset:39936
	s_add_u32 s3, s19, 7
	s_and_b32 s3, s3, 7
	s_lshl_b32 s57, s3, 10
	s_add_u32 s48, s57, s22
	s_add_u32 s49, s48, 0x2000
	s_add_u32 s50, s48, 0x4000
	s_add_u32 s51, s48, 0x6000
	s_add_u32 s52, s48, 0x8000
	s_add_u32 s53, s48, 0xa000
	s_add_u32 s54, s48, 0xc000
	s_add_u32 s55, s48, 0xe000
	s_lshl_b32 s56, s3, 15
	s_add_u32 s56, s56, s23
	buffer_load_dwordx4 v[120:123], v1, s[4:7], s48 offen nt
	buffer_load_dwordx4 v[124:127], v1, s[4:7], s49 offen nt
	buffer_load_dwordx4 v[128:131], v1, s[4:7], s50 offen nt
	buffer_load_dwordx4 v[132:135], v1, s[4:7], s51 offen nt
	buffer_load_dwordx4 v[136:139], v1, s[4:7], s52 offen nt
	buffer_load_dwordx4 v[140:143], v1, s[4:7], s53 offen nt
	buffer_load_dwordx4 v[144:147], v1, s[4:7], s54 offen nt
	buffer_load_dwordx4 v[148:151], v1, s[4:7], s55 offen nt
	buffer_load_dwordx4 v[168:171], v1, s[8:11], s56 offen
	buffer_load_dwordx4 v[172:175], v1, s[8:11], s56 offen offset:1024
	buffer_load_dwordx4 v[176:179], v1, s[8:11], s56 offen offset:2048
	buffer_load_dwordx4 v[180:183], v1, s[8:11], s56 offen offset:3072
	s_waitcnt vmcnt(12)
	v_pk_mul_f32 v[24:25], v[16:17], s[32:33] op_sel_hi:[1,0]
	v_pk_mul_f32 v[26:27], v[18:19], s[32:33] op_sel_hi:[1,0]
	v_pk_mul_f32 v[28:29], v[20:21], s[40:41] op_sel_hi:[1,0]
	v_pk_mul_f32 v[30:31], v[22:23], s[40:41] op_sel_hi:[1,0]
	v_cmp_lt_i32_e64 s[60:61], 0, v88
	v_cmp_lt_i32_e64 s[62:63], 0, v89
	v_cmp_lt_i32_e64 s[64:65], 0, v90
	v_cmp_lt_i32_e64 s[66:67], 0, v91
	v_max_f32_e32 v24, v24, v28
	v_max_f32_e32 v25, v25, v29
	v_max_f32_e32 v26, v26, v30
	v_max_f32_e32 v27, v27, v31
	v_cndmask_b32_e64 v24, 0, v24, s[60:61]
	v_cndmask_b32_e64 v25, 0, v25, s[62:63]
	v_cndmask_b32_e64 v26, 0, v26, s[64:65]
	v_cndmask_b32_e64 v27, 0, v27, s[66:67]
	v_cvt_pkrtz_f16_f32 v32, v24, v25
	v_cvt_pkrtz_f16_f32 v33, v26, v27
	s_waitcnt lgkmcnt(0)
	v_pk_mul_f32 v[24:25], v[16:17], s[32:33] op_sel:[0,1] op_sel_hi:[1,1]
	v_pk_mul_f32 v[26:27], v[18:19], s[32:33] op_sel:[0,1] op_sel_hi:[1,1]
	v_pk_mul_f32 v[28:29], v[20:21], s[40:41] op_sel:[0,1] op_sel_hi:[1,1]
	v_pk_mul_f32 v[30:31], v[22:23], s[40:41] op_sel:[0,1] op_sel_hi:[1,1]
	v_mfma_f32_32x32x16_f16 v[40:55], v[184:187], v[200:203], v[40:55]
	v_cmp_lt_i32_e64 s[60:61], 0, v92
	v_cmp_lt_i32_e64 s[62:63], 0, v93
	v_cmp_lt_i32_e64 s[64:65], 0, v94
	v_cmp_lt_i32_e64 s[66:67], 0, v95
	v_max_f32_e32 v24, v24, v28
	v_max_f32_e32 v25, v25, v29
	v_max_f32_e32 v26, v26, v30
	v_max_f32_e32 v27, v27, v31
	v_cndmask_b32_e64 v24, 0, v24, s[60:61]
	v_cndmask_b32_e64 v25, 0, v25, s[62:63]
	v_cndmask_b32_e64 v26, 0, v26, s[64:65]
	v_cndmask_b32_e64 v27, 0, v27, s[66:67]
	v_mfma_f32_32x32x16_f16 v[56:71], v[184:187], v[204:207], v[56:71]
	v_cvt_pkrtz_f16_f32 v34, v24, v25
	v_cvt_pkrtz_f16_f32 v35, v26, v27
	ds_write2_b64 v3, v[32:33], v[34:35] offset0:0 offset1:66
	v_pk_mul_f32 v[24:25], v[16:17], s[34:35] op_sel_hi:[1,0]
	v_pk_mul_f32 v[26:27], v[18:19], s[34:35] op_sel_hi:[1,0]
	v_pk_mul_f32 v[28:29], v[20:21], s[42:43] op_sel_hi:[1,0]
	v_pk_mul_f32 v[30:31], v[22:23], s[42:43] op_sel_hi:[1,0]
	v_mfma_f32_32x32x16_f16 v[72:87], v[184:187], v[12:15], v[72:87]
	v_cmp_lt_i32_e64 s[60:61], 0, v96
	v_cmp_lt_i32_e64 s[62:63], 0, v97
	v_cmp_lt_i32_e64 s[64:65], 0, v98
	v_cmp_lt_i32_e64 s[66:67], 0, v99
	v_max_f32_e32 v24, v24, v28
	v_max_f32_e32 v25, v25, v29
	v_max_f32_e32 v26, v26, v30
	v_max_f32_e32 v27, v27, v31
	v_cndmask_b32_e64 v24, 0, v24, s[60:61]
	v_cndmask_b32_e64 v25, 0, v25, s[62:63]
	v_cndmask_b32_e64 v26, 0, v26, s[64:65]
	v_cndmask_b32_e64 v27, 0, v27, s[66:67]
	v_mfma_f32_32x32x16_f16 v[40:55], v[188:191], v[208:211], v[40:55]
	v_cvt_pkrtz_f16_f32 v32, v24, v25
	v_cvt_pkrtz_f16_f32 v33, v26, v27
	v_pk_mul_f32 v[24:25], v[16:17], s[34:35] op_sel:[0,1] op_sel_hi:[1,1]
	v_pk_mul_f32 v[26:27], v[18:19], s[34:35] op_sel:[0,1] op_sel_hi:[1,1]
	v_pk_mul_f32 v[28:29], v[20:21], s[42:43] op_sel:[0,1] op_sel_hi:[1,1]
	v_pk_mul_f32 v[30:31], v[22:23], s[42:43] op_sel:[0,1] op_sel_hi:[1,1]
	v_mfma_f32_32x32x16_f16 v[56:71], v[188:191], v[212:215], v[56:71]
	v_cmp_lt_i32_e64 s[60:61], 0, v100
	v_cmp_lt_i32_e64 s[62:63], 0, v101
	v_cmp_lt_i32_e64 s[64:65], 0, v102
	v_cmp_lt_i32_e64 s[66:67], 0, v103
	v_max_f32_e32 v24, v24, v28
	v_max_f32_e32 v25, v25, v29
	v_max_f32_e32 v26, v26, v30
	v_max_f32_e32 v27, v27, v31
	v_cndmask_b32_e64 v24, 0, v24, s[60:61]
	v_cndmask_b32_e64 v25, 0, v25, s[62:63]
	v_cndmask_b32_e64 v26, 0, v26, s[64:65]
	v_cndmask_b32_e64 v27, 0, v27, s[66:67]
	v_mfma_f32_32x32x16_f16 v[72:87], v[188:191], v[12:15], v[72:87]
	v_cvt_pkrtz_f16_f32 v34, v24, v25
	v_cvt_pkrtz_f16_f32 v35, v26, v27
	ds_write2_b64 v3, v[32:33], v[34:35] offset0:132 offset1:198
	v_pk_mul_f32 v[24:25], v[16:17], s[36:37] op_sel_hi:[1,0]
	v_pk_mul_f32 v[26:27], v[18:19], s[36:37] op_sel_hi:[1,0]
	v_pk_mul_f32 v[28:29], v[20:21], s[44:45] op_sel_hi:[1,0]
	v_pk_mul_f32 v[30:31], v[22:23], s[44:45] op_sel_hi:[1,0]
	v_mfma_f32_32x32x16_f16 v[40:55], v[192:195], v[216:219], v[40:55]
	v_cmp_lt_i32_e64 s[60:61], 0, v104
	v_cmp_lt_i32_e64 s[62:63], 0, v105
	v_cmp_lt_i32_e64 s[64:65], 0, v106
	v_cmp_lt_i32_e64 s[66:67], 0, v107
	v_max_f32_e32 v24, v24, v28
	v_max_f32_e32 v25, v25, v29
	v_max_f32_e32 v26, v26, v30
	v_max_f32_e32 v27, v27, v31
	v_cndmask_b32_e64 v24, 0, v24, s[60:61]
	v_cndmask_b32_e64 v25, 0, v25, s[62:63]
	v_cndmask_b32_e64 v26, 0, v26, s[64:65]
	v_cndmask_b32_e64 v27, 0, v27, s[66:67]
	v_mfma_f32_32x32x16_f16 v[56:71], v[192:195], v[220:223], v[56:71]
	v_cvt_pkrtz_f16_f32 v32, v24, v25
	v_cvt_pkrtz_f16_f32 v33, v26, v27
	v_pk_mul_f32 v[24:25], v[16:17], s[36:37] op_sel:[0,1] op_sel_hi:[1,1]
	v_pk_mul_f32 v[26:27], v[18:19], s[36:37] op_sel:[0,1] op_sel_hi:[1,1]
	v_pk_mul_f32 v[28:29], v[20:21], s[44:45] op_sel:[0,1] op_sel_hi:[1,1]
	v_pk_mul_f32 v[30:31], v[22:23], s[44:45] op_sel:[0,1] op_sel_hi:[1,1]
	v_mfma_f32_32x32x16_f16 v[72:87], v[192:195], v[12:15], v[72:87]
	v_cmp_lt_i32_e64 s[60:61], 0, v108
	v_cmp_lt_i32_e64 s[62:63], 0, v109
	v_cmp_lt_i32_e64 s[64:65], 0, v110
	v_cmp_lt_i32_e64 s[66:67], 0, v111
	v_max_f32_e32 v24, v24, v28
	v_max_f32_e32 v25, v25, v29
	v_max_f32_e32 v26, v26, v30
	v_max_f32_e32 v27, v27, v31
	v_cndmask_b32_e64 v24, 0, v24, s[60:61]
	v_cndmask_b32_e64 v25, 0, v25, s[62:63]
	v_cndmask_b32_e64 v26, 0, v26, s[64:65]
	v_cndmask_b32_e64 v27, 0, v27, s[66:67]
	v_mfma_f32_32x32x16_f16 v[40:55], v[196:199], v[224:227], v[40:55]
	v_cvt_pkrtz_f16_f32 v34, v24, v25
	v_cvt_pkrtz_f16_f32 v35, v26, v27
	ds_write2_b64 v4, v[32:33], v[34:35] offset0:0 offset1:66
	v_pk_mul_f32 v[24:25], v[16:17], s[38:39] op_sel_hi:[1,0]
	v_pk_mul_f32 v[26:27], v[18:19], s[38:39] op_sel_hi:[1,0]
	v_pk_mul_f32 v[28:29], v[20:21], s[46:47] op_sel_hi:[1,0]
	v_pk_mul_f32 v[30:31], v[22:23], s[46:47] op_sel_hi:[1,0]
	v_mfma_f32_32x32x16_f16 v[56:71], v[196:199], v[228:231], v[56:71]
	v_cmp_lt_i32_e64 s[60:61], 0, v112
	v_cmp_lt_i32_e64 s[62:63], 0, v113
	v_cmp_lt_i32_e64 s[64:65], 0, v114
	v_cmp_lt_i32_e64 s[66:67], 0, v115
	v_max_f32_e32 v24, v24, v28
	v_max_f32_e32 v25, v25, v29
	v_max_f32_e32 v26, v26, v30
	v_max_f32_e32 v27, v27, v31
	v_cndmask_b32_e64 v24, 0, v24, s[60:61]
	v_cndmask_b32_e64 v25, 0, v25, s[62:63]
	v_cndmask_b32_e64 v26, 0, v26, s[64:65]
	v_cndmask_b32_e64 v27, 0, v27, s[66:67]
	v_cvt_pkrtz_f16_f32 v32, v24, v25
	v_cvt_pkrtz_f16_f32 v33, v26, v27
	v_pk_mul_f32 v[24:25], v[16:17], s[38:39] op_sel:[0,1] op_sel_hi:[1,1]
	v_pk_mul_f32 v[26:27], v[18:19], s[38:39] op_sel:[0,1] op_sel_hi:[1,1]
	v_pk_mul_f32 v[28:29], v[20:21], s[46:47] op_sel:[0,1] op_sel_hi:[1,1]
	v_pk_mul_f32 v[30:31], v[22:23], s[46:47] op_sel:[0,1] op_sel_hi:[1,1]
	v_mfma_f32_32x32x16_f16 v[72:87], v[196:199], v[12:15], v[72:87]
	v_cmp_lt_i32_e64 s[60:61], 0, v116
	v_cmp_lt_i32_e64 s[62:63], 0, v117
	v_cmp_lt_i32_e64 s[64:65], 0, v118
	v_cmp_lt_i32_e64 s[66:67], 0, v119
	v_max_f32_e32 v24, v24, v28
	v_max_f32_e32 v25, v25, v29
	v_max_f32_e32 v26, v26, v30
	v_max_f32_e32 v27, v27, v31
	v_cndmask_b32_e64 v24, 0, v24, s[60:61]
	v_cndmask_b32_e64 v25, 0, v25, s[62:63]
	v_cndmask_b32_e64 v26, 0, v26, s[64:65]
	v_cndmask_b32_e64 v27, 0, v27, s[66:67]
	v_cvt_pkrtz_f16_f32 v34, v24, v25
	v_cvt_pkrtz_f16_f32 v35, v26, v27
	ds_write2_b64 v4, v[32:33], v[34:35] offset0:132 offset1:198
	ds_write_b128 v9, v[152:155] offset:0
	ds_write_b128 v9, v[156:159] offset:1024
	ds_write_b128 v9, v[160:163] offset:2048
	ds_write_b128 v9, v[164:167] offset:3072
	s_add_u32 s3, s19, 7
	s_and_b32 s3, s3, 7
	s_lshl_b32 s3, s3, 10
	v_add_u32_e32 v11, s3, v10
	ds_read_b128 v[16:19], v11
	ds_read_b128 v[20:23], v11 offset:8192
	s_waitcnt lgkmcnt(0)
	s_barrier
	ds_read_b128 v[184:187], v7 offset:0
	ds_read_b128 v[200:203], v8 offset:0
	ds_read_b128 v[204:207], v8 offset:1024
	ds_read_b128 v[188:191], v7 offset:32
	ds_read_b128 v[208:211], v8 offset:2048
	ds_read_b128 v[212:215], v8 offset:3072
	ds_read_b128 v[192:195], v7 offset:64
	ds_read_b128 v[216:219], v8 offset:4096
	ds_read_b128 v[220:223], v8 offset:5120
	ds_read_b128 v[196:199], v7 offset:96
	ds_read_b128 v[224:227], v8 offset:6144
	ds_read_b128 v[228:231], v8 offset:7168
	s_waitcnt vmcnt(0)
	v_pk_mul_f32 v[24:25], v[16:17], s[32:33] op_sel_hi:[1,0]
	v_pk_mul_f32 v[26:27], v[18:19], s[32:33] op_sel_hi:[1,0]
	v_pk_mul_f32 v[28:29], v[20:21], s[40:41] op_sel_hi:[1,0]
	v_pk_mul_f32 v[30:31], v[22:23], s[40:41] op_sel_hi:[1,0]
	v_cmp_lt_i32_e64 s[60:61], 0, v120
	v_cmp_lt_i32_e64 s[62:63], 0, v121
	v_cmp_lt_i32_e64 s[64:65], 0, v122
	v_cmp_lt_i32_e64 s[66:67], 0, v123
	v_max_f32_e32 v24, v24, v28
	v_max_f32_e32 v25, v25, v29
	v_max_f32_e32 v26, v26, v30
	v_max_f32_e32 v27, v27, v31
	v_cndmask_b32_e64 v24, 0, v24, s[60:61]
	v_cndmask_b32_e64 v25, 0, v25, s[62:63]
	v_cndmask_b32_e64 v26, 0, v26, s[64:65]
	v_cndmask_b32_e64 v27, 0, v27, s[66:67]
	v_cvt_pkrtz_f16_f32 v32, v24, v25
	v_cvt_pkrtz_f16_f32 v33, v26, v27
	s_waitcnt lgkmcnt(0)
	v_pk_mul_f32 v[24:25], v[16:17], s[32:33] op_sel:[0,1] op_sel_hi:[1,1]
	v_pk_mul_f32 v[26:27], v[18:19], s[32:33] op_sel:[0,1] op_sel_hi:[1,1]
	v_pk_mul_f32 v[28:29], v[20:21], s[40:41] op_sel:[0,1] op_sel_hi:[1,1]
	v_pk_mul_f32 v[30:31], v[22:23], s[40:41] op_sel:[0,1] op_sel_hi:[1,1]
	v_mfma_f32_32x32x16_f16 v[40:55], v[184:187], v[200:203], v[40:55]
	v_cmp_lt_i32_e64 s[60:61], 0, v124
	v_cmp_lt_i32_e64 s[62:63], 0, v125
	v_cmp_lt_i32_e64 s[64:65], 0, v126
	v_cmp_lt_i32_e64 s[66:67], 0, v127
	v_max_f32_e32 v24, v24, v28
	v_max_f32_e32 v25, v25, v29
	v_max_f32_e32 v26, v26, v30
	v_max_f32_e32 v27, v27, v31
	v_cndmask_b32_e64 v24, 0, v24, s[60:61]
	v_cndmask_b32_e64 v25, 0, v25, s[62:63]
	v_cndmask_b32_e64 v26, 0, v26, s[64:65]
	v_cndmask_b32_e64 v27, 0, v27, s[66:67]
	v_mfma_f32_32x32x16_f16 v[56:71], v[184:187], v[204:207], v[56:71]
	v_cvt_pkrtz_f16_f32 v34, v24, v25
	v_cvt_pkrtz_f16_f32 v35, v26, v27
	ds_write2_b64 v5, v[32:33], v[34:35] offset0:0 offset1:66
	v_pk_mul_f32 v[24:25], v[16:17], s[34:35] op_sel_hi:[1,0]
	v_pk_mul_f32 v[26:27], v[18:19], s[34:35] op_sel_hi:[1,0]
	v_pk_mul_f32 v[28:29], v[20:21], s[42:43] op_sel_hi:[1,0]
	v_pk_mul_f32 v[30:31], v[22:23], s[42:43] op_sel_hi:[1,0]
	v_mfma_f32_32x32x16_f16 v[72:87], v[184:187], v[12:15], v[72:87]
	v_cmp_lt_i32_e64 s[60:61], 0, v128
	v_cmp_lt_i32_e64 s[62:63], 0, v129
	v_cmp_lt_i32_e64 s[64:65], 0, v130
	v_cmp_lt_i32_e64 s[66:67], 0, v131
	v_max_f32_e32 v24, v24, v28
	v_max_f32_e32 v25, v25, v29
	v_max_f32_e32 v26, v26, v30
	v_max_f32_e32 v27, v27, v31
	v_cndmask_b32_e64 v24, 0, v24, s[60:61]
	v_cndmask_b32_e64 v25, 0, v25, s[62:63]
	v_cndmask_b32_e64 v26, 0, v26, s[64:65]
	v_cndmask_b32_e64 v27, 0, v27, s[66:67]
	v_mfma_f32_32x32x16_f16 v[40:55], v[188:191], v[208:211], v[40:55]
	v_cvt_pkrtz_f16_f32 v32, v24, v25
	v_cvt_pkrtz_f16_f32 v33, v26, v27
	v_pk_mul_f32 v[24:25], v[16:17], s[34:35] op_sel:[0,1] op_sel_hi:[1,1]
	v_pk_mul_f32 v[26:27], v[18:19], s[34:35] op_sel:[0,1] op_sel_hi:[1,1]
	v_pk_mul_f32 v[28:29], v[20:21], s[42:43] op_sel:[0,1] op_sel_hi:[1,1]
	v_pk_mul_f32 v[30:31], v[22:23], s[42:43] op_sel:[0,1] op_sel_hi:[1,1]
	v_mfma_f32_32x32x16_f16 v[56:71], v[188:191], v[212:215], v[56:71]
	v_cmp_lt_i32_e64 s[60:61], 0, v132
	v_cmp_lt_i32_e64 s[62:63], 0, v133
	v_cmp_lt_i32_e64 s[64:65], 0, v134
	v_cmp_lt_i32_e64 s[66:67], 0, v135
	v_max_f32_e32 v24, v24, v28
	v_max_f32_e32 v25, v25, v29
	v_max_f32_e32 v26, v26, v30
	v_max_f32_e32 v27, v27, v31
	v_cndmask_b32_e64 v24, 0, v24, s[60:61]
	v_cndmask_b32_e64 v25, 0, v25, s[62:63]
	v_cndmask_b32_e64 v26, 0, v26, s[64:65]
	v_cndmask_b32_e64 v27, 0, v27, s[66:67]
	v_mfma_f32_32x32x16_f16 v[72:87], v[188:191], v[12:15], v[72:87]
	v_cvt_pkrtz_f16_f32 v34, v24, v25
	v_cvt_pkrtz_f16_f32 v35, v26, v27
	ds_write2_b64 v5, v[32:33], v[34:35] offset0:132 offset1:198
	v_pk_mul_f32 v[24:25], v[16:17], s[36:37] op_sel_hi:[1,0]
	v_pk_mul_f32 v[26:27], v[18:19], s[36:37] op_sel_hi:[1,0]
	v_pk_mul_f32 v[28:29], v[20:21], s[44:45] op_sel_hi:[1,0]
	v_pk_mul_f32 v[30:31], v[22:23], s[44:45] op_sel_hi:[1,0]
	v_mfma_f32_32x32x16_f16 v[40:55], v[192:195], v[216:219], v[40:55]
	v_cmp_lt_i32_e64 s[60:61], 0, v136
	v_cmp_lt_i32_e64 s[62:63], 0, v137
	v_cmp_lt_i32_e64 s[64:65], 0, v138
	v_cmp_lt_i32_e64 s[66:67], 0, v139
	v_max_f32_e32 v24, v24, v28
	v_max_f32_e32 v25, v25, v29
	v_max_f32_e32 v26, v26, v30
	v_max_f32_e32 v27, v27, v31
	v_cndmask_b32_e64 v24, 0, v24, s[60:61]
	v_cndmask_b32_e64 v25, 0, v25, s[62:63]
	v_cndmask_b32_e64 v26, 0, v26, s[64:65]
	v_cndmask_b32_e64 v27, 0, v27, s[66:67]
	v_mfma_f32_32x32x16_f16 v[56:71], v[192:195], v[220:223], v[56:71]
	v_cvt_pkrtz_f16_f32 v32, v24, v25
	v_cvt_pkrtz_f16_f32 v33, v26, v27
	v_pk_mul_f32 v[24:25], v[16:17], s[36:37] op_sel:[0,1] op_sel_hi:[1,1]
	v_pk_mul_f32 v[26:27], v[18:19], s[36:37] op_sel:[0,1] op_sel_hi:[1,1]
	v_pk_mul_f32 v[28:29], v[20:21], s[44:45] op_sel:[0,1] op_sel_hi:[1,1]
	v_pk_mul_f32 v[30:31], v[22:23], s[44:45] op_sel:[0,1] op_sel_hi:[1,1]
	v_mfma_f32_32x32x16_f16 v[72:87], v[192:195], v[12:15], v[72:87]
	v_cmp_lt_i32_e64 s[60:61], 0, v140
	v_cmp_lt_i32_e64 s[62:63], 0, v141
	v_cmp_lt_i32_e64 s[64:65], 0, v142
	v_cmp_lt_i32_e64 s[66:67], 0, v143
	v_max_f32_e32 v24, v24, v28
	v_max_f32_e32 v25, v25, v29
	v_max_f32_e32 v26, v26, v30
	v_max_f32_e32 v27, v27, v31
	v_cndmask_b32_e64 v24, 0, v24, s[60:61]
	v_cndmask_b32_e64 v25, 0, v25, s[62:63]
	v_cndmask_b32_e64 v26, 0, v26, s[64:65]
	v_cndmask_b32_e64 v27, 0, v27, s[66:67]
	v_mfma_f32_32x32x16_f16 v[40:55], v[196:199], v[224:227], v[40:55]
	v_cvt_pkrtz_f16_f32 v34, v24, v25
	v_cvt_pkrtz_f16_f32 v35, v26, v27
	ds_write2_b64 v6, v[32:33], v[34:35] offset0:0 offset1:66
	v_pk_mul_f32 v[24:25], v[16:17], s[38:39] op_sel_hi:[1,0]
	v_pk_mul_f32 v[26:27], v[18:19], s[38:39] op_sel_hi:[1,0]
	v_pk_mul_f32 v[28:29], v[20:21], s[46:47] op_sel_hi:[1,0]
	v_pk_mul_f32 v[30:31], v[22:23], s[46:47] op_sel_hi:[1,0]
	v_mfma_f32_32x32x16_f16 v[56:71], v[196:199], v[228:231], v[56:71]
	v_cmp_lt_i32_e64 s[60:61], 0, v144
	v_cmp_lt_i32_e64 s[62:63], 0, v145
	v_cmp_lt_i32_e64 s[64:65], 0, v146
	v_cmp_lt_i32_e64 s[66:67], 0, v147
	v_max_f32_e32 v24, v24, v28
	v_max_f32_e32 v25, v25, v29
	v_max_f32_e32 v26, v26, v30
	v_max_f32_e32 v27, v27, v31
	v_cndmask_b32_e64 v24, 0, v24, s[60:61]
	v_cndmask_b32_e64 v25, 0, v25, s[62:63]
	v_cndmask_b32_e64 v26, 0, v26, s[64:65]
	v_cndmask_b32_e64 v27, 0, v27, s[66:67]
	v_cvt_pkrtz_f16_f32 v32, v24, v25
	v_cvt_pkrtz_f16_f32 v33, v26, v27
	v_pk_mul_f32 v[24:25], v[16:17], s[38:39] op_sel:[0,1] op_sel_hi:[1,1]
	v_pk_mul_f32 v[26:27], v[18:19], s[38:39] op_sel:[0,1] op_sel_hi:[1,1]
	v_pk_mul_f32 v[28:29], v[20:21], s[46:47] op_sel:[0,1] op_sel_hi:[1,1]
	v_pk_mul_f32 v[30:31], v[22:23], s[46:47] op_sel:[0,1] op_sel_hi:[1,1]
	v_mfma_f32_32x32x16_f16 v[72:87], v[196:199], v[12:15], v[72:87]
	v_cmp_lt_i32_e64 s[60:61], 0, v148
	v_cmp_lt_i32_e64 s[62:63], 0, v149
	v_cmp_lt_i32_e64 s[64:65], 0, v150
	v_cmp_lt_i32_e64 s[66:67], 0, v151
	v_max_f32_e32 v24, v24, v28
	v_max_f32_e32 v25, v25, v29
	v_max_f32_e32 v26, v26, v30
	v_max_f32_e32 v27, v27, v31
	v_cndmask_b32_e64 v24, 0, v24, s[60:61]
	v_cndmask_b32_e64 v25, 0, v25, s[62:63]
	v_cndmask_b32_e64 v26, 0, v26, s[64:65]
	v_cndmask_b32_e64 v27, 0, v27, s[66:67]
	v_cvt_pkrtz_f16_f32 v34, v24, v25
	v_cvt_pkrtz_f16_f32 v35, v26, v27
	ds_write2_b64 v6, v[32:33], v[34:35] offset0:132 offset1:198
	ds_write_b128 v9, v[168:171] offset:32768
	ds_write_b128 v9, v[172:175] offset:33792
	ds_write_b128 v9, v[176:179] offset:34816
	ds_write_b128 v9, v[180:183] offset:35840
	s_waitcnt lgkmcnt(0)
	s_barrier
	ds_read_b128 v[184:187], v7 offset:33792
	ds_read_b128 v[200:203], v8 offset:32768
	ds_read_b128 v[204:207], v8 offset:33792
	ds_read_b128 v[188:191], v7 offset:33824
	ds_read_b128 v[208:211], v8 offset:34816
	ds_read_b128 v[212:215], v8 offset:35840
	ds_read_b128 v[192:195], v7 offset:33856
	ds_read_b128 v[216:219], v8 offset:36864
	ds_read_b128 v[220:223], v8 offset:37888
	ds_read_b128 v[196:199], v7 offset:33888
	ds_read_b128 v[224:227], v8 offset:38912
	ds_read_b128 v[228:231], v8 offset:39936
	s_waitcnt lgkmcnt(0)
	v_mfma_f32_32x32x16_f16 v[40:55], v[184:187], v[200:203], v[40:55]
	v_mfma_f32_32x32x16_f16 v[56:71], v[184:187], v[204:207], v[56:71]
	v_mfma_f32_32x32x16_f16 v[72:87], v[184:187], v[12:15], v[72:87]
	v_mfma_f32_32x32x16_f16 v[40:55], v[188:191], v[208:211], v[40:55]
	v_mfma_f32_32x32x16_f16 v[56:71], v[188:191], v[212:215], v[56:71]
	v_mfma_f32_32x32x16_f16 v[72:87], v[188:191], v[12:15], v[72:87]
	v_mfma_f32_32x32x16_f16 v[40:55], v[192:195], v[216:219], v[40:55]
	v_mfma_f32_32x32x16_f16 v[56:71], v[192:195], v[220:223], v[56:71]
	v_mfma_f32_32x32x16_f16 v[72:87], v[192:195], v[12:15], v[72:87]
	v_mfma_f32_32x32x16_f16 v[40:55], v[196:199], v[224:227], v[40:55]
	v_mfma_f32_32x32x16_f16 v[56:71], v[196:199], v[228:231], v[56:71]
	v_mfma_f32_32x32x16_f16 v[72:87], v[196:199], v[12:15], v[72:87]
	s_nop 11
	s_cmp_eq_u32 s21, 0
	s_cbranch_scc0 .Lgm_red_not0
	s_lshl_b32 s3, s20, 2
	s_add_u32 s3, s3, 1
	s_mul_i32 s57, s3, 0x2400
	s_cmp_ge_u32 s3, 3
	s_cselect_b32 s58, 0x9c00, 0
	s_add_u32 s57, s57, s58
	v_add_u32_e32 v36, s57, v1
	s_lshl_b32 s3, s20, 2
	s_add_u32 s3, s3, 2
	s_mul_i32 s57, s3, 0x2400
	s_cmp_ge_u32 s3, 3
	s_cselect_b32 s58, 0x9c00, 0
	s_add_u32 s57, s57, s58
	v_add_u32_e32 v37, s57, v1
	s_lshl_b32 s3, s20, 2
	s_add_u32 s3, s3, 3
	s_mul_i32 s57, s3, 0x2400
	s_cmp_ge_u32 s3, 3
	s_cselect_b32 s58, 0x9c00, 0
	s_add_u32 s57, s57, s58
	v_add_u32_e32 v38, s57, v1
	ds_write_b128 v36, v[44:47] offset:0
	ds_write_b128 v36, v[60:63] offset:1024
	ds_write_b128 v36, v[76:79] offset:2048
	ds_write_b128 v37, v[48:51] offset:0
	ds_write_b128 v37, v[64:67] offset:1024
	ds_write_b128 v37, v[80:83] offset:2048
	ds_write_b128 v38, v[52:55] offset:0
	ds_write_b128 v38, v[68:71] offset:1024
	ds_write_b128 v38, v[84:87] offset:2048
	s_waitcnt lgkmcnt(0)
	s_barrier
	s_mov_b32 s3, s16
	s_mul_i32 s57, s3, 0x2400
	s_cmp_ge_u32 s3, 3
	s_cselect_b32 s58, 0x9c00, 0
	s_add_u32 s57, s57, s58
	v_add_u32_e32 v36, s57, v1
	ds_read_b128 v[88:91], v36 offset:0
	ds_read_b128 v[92:95], v36 offset:1024
	ds_read_b128 v[96:99], v36 offset:2048
	ds_read_b128 v[100:103], v36 offset:3072
	ds_read_b128 v[104:107], v36 offset:4096
	ds_read_b128 v[108:111], v36 offset:5120
	ds_read_b128 v[112:115], v36 offset:6144
	ds_read_b128 v[116:119], v36 offset:7168
	ds_read_b128 v[120:123], v36 offset:8192
	s_waitcnt lgkmcnt(0)
	v_add_f32_e32 v40, v40, v88
	v_add_f32_e32 v41, v41, v89
	v_add_f32_e32 v42, v42, v90
	v_add_f32_e32 v43, v43, v91
	v_add_f32_e32 v40, v40, v100
	v_add_f32_e32 v41, v41, v101
	v_add_f32_e32 v42, v42, v102
	v_add_f32_e32 v43, v43, v103
	v_add_f32_e32 v40, v40, v112
	v_add_f32_e32 v41, v41, v113
	v_add_f32_e32 v42, v42, v114
	v_add_f32_e32 v43, v43, v115
	v_add_f32_e32 v44, v56, v92
	v_add_f32_e32 v45, v57, v93
	v_add_f32_e32 v46, v58, v94
	v_add_f32_e32 v47, v59, v95
	v_add_f32_e32 v44, v44, v104
	v_add_f32_e32 v45, v45, v105
	v_add_f32_e32 v46, v46, v106
	v_add_f32_e32 v47, v47, v107
	v_add_f32_e32 v44, v44, v116
	v_add_f32_e32 v45, v45, v117
	v_add_f32_e32 v46, v46, v118
	v_add_f32_e32 v47, v47, v119
	v_add_f32_e32 v48, v72, v96
	v_add_f32_e32 v49, v73, v97
	v_add_f32_e32 v50, v74, v98
	v_add_f32_e32 v51, v75, v99
	v_add_f32_e32 v48, v48, v108
	v_add_f32_e32 v49, v49, v109
	v_add_f32_e32 v50, v50, v110
	v_add_f32_e32 v51, v51, v111
	v_add_f32_e32 v48, v48, v120
	v_add_f32_e32 v49, v49, v121
	v_add_f32_e32 v50, v50, v122
	v_add_f32_e32 v51, v51, v123
	s_branch .Lgm_red_done
.Lgm_red_not0:
	s_cmp_eq_u32 s21, 1
	s_cbranch_scc0 .Lgm_red_not1
	s_lshl_b32 s3, s20, 2
	s_mul_i32 s57, s3, 0x2400
	s_cmp_ge_u32 s3, 3
	s_cselect_b32 s58, 0x9c00, 0
	s_add_u32 s57, s57, s58
	v_add_u32_e32 v36, s57, v1
	s_lshl_b32 s3, s20, 2
	s_add_u32 s3, s3, 2
	s_mul_i32 s57, s3, 0x2400
	s_cmp_ge_u32 s3, 3
	s_cselect_b32 s58, 0x9c00, 0
	s_add_u32 s57, s57, s58
	v_add_u32_e32 v37, s57, v1
	s_lshl_b32 s3, s20, 2
	s_add_u32 s3, s3, 3
	s_mul_i32 s57, s3, 0x2400
	s_cmp_ge_u32 s3, 3
	s_cselect_b32 s58, 0x9c00, 0
	s_add_u32 s57, s57, s58
	v_add_u32_e32 v38, s57, v1
	ds_write_b128 v36, v[40:43] offset:0
	ds_write_b128 v36, v[56:59] offset:1024
	ds_write_b128 v36, v[72:75] offset:2048
	ds_write_b128 v37, v[48:51] offset:3072
	ds_write_b128 v37, v[64:67] offset:4096
	ds_write_b128 v37, v[80:83] offset:5120
	ds_write_b128 v38, v[52:55] offset:3072
	ds_write_b128 v38, v[68:71] offset:4096
	ds_write_b128 v38, v[84:87] offset:5120
	s_waitcnt lgkmcnt(0)
	s_barrier
	s_mov_b32 s3, s16
	s_mul_i32 s57, s3, 0x2400
	s_cmp_ge_u32 s3, 3
	s_cselect_b32 s58, 0x9c00, 0
	s_add_u32 s57, s57, s58
	v_add_u32_e32 v36, s57, v1
	ds_read_b128 v[88:91], v36 offset:0
	ds_read_b128 v[92:95], v36 offset:1024
	ds_read_b128 v[96:99], v36 offset:2048
	ds_read_b128 v[100:103], v36 offset:3072
	ds_read_b128 v[104:107], v36 offset:4096
	ds_read_b128 v[108:111], v36 offset:5120
	ds_read_b128 v[112:115], v36 offset:6144
	ds_read_b128 v[116:119], v36 offset:7168
	ds_read_b128 v[120:123], v36 offset:8192
	s_waitcnt lgkmcnt(0)
	v_add_f32_e32 v40, v44, v88
	v_add_f32_e32 v41, v45, v89
	v_add_f32_e32 v42, v46, v90
	v_add_f32_e32 v43, v47, v91
	v_add_f32_e32 v40, v40, v100
	v_add_f32_e32 v41, v41, v101
	v_add_f32_e32 v42, v42, v102
	v_add_f32_e32 v43, v43, v103
	v_add_f32_e32 v40, v40, v112
	v_add_f32_e32 v41, v41, v113
	v_add_f32_e32 v42, v42, v114
	v_add_f32_e32 v43, v43, v115
	v_add_f32_e32 v44, v60, v92
	v_add_f32_e32 v45, v61, v93
	v_add_f32_e32 v46, v62, v94
	v_add_f32_e32 v47, v63, v95
	v_add_f32_e32 v44, v44, v104
	v_add_f32_e32 v45, v45, v105
	v_add_f32_e32 v46, v46, v106
	v_add_f32_e32 v47, v47, v107
	v_add_f32_e32 v44, v44, v116
	v_add_f32_e32 v45, v45, v117
	v_add_f32_e32 v46, v46, v118
	v_add_f32_e32 v47, v47, v119
	v_add_f32_e32 v48, v76, v96
	v_add_f32_e32 v49, v77, v97
	v_add_f32_e32 v50, v78, v98
	v_add_f32_e32 v51, v79, v99
	v_add_f32_e32 v48, v48, v108
	v_add_f32_e32 v49, v49, v109
	v_add_f32_e32 v50, v50, v110
	v_add_f32_e32 v51, v51, v111
	v_add_f32_e32 v48, v48, v120
	v_add_f32_e32 v49, v49, v121
	v_add_f32_e32 v50, v50, v122
	v_add_f32_e32 v51, v51, v123
	s_branch .Lgm_red_done
.Lgm_red_not1:
	s_cmp_eq_u32 s21, 2
	s_cbranch_scc0 .Lgm_red_not2
	s_lshl_b32 s3, s20, 2
	s_mul_i32 s57, s3, 0x2400
	s_cmp_ge_u32 s3, 3
	s_cselect_b32 s58, 0x9c00, 0
	s_add_u32 s57, s57, s58
	v_add_u32_e32 v36, s57, v1
	s_lshl_b32 s3, s20, 2
	s_add_u32 s3, s3, 1
	s_mul_i32 s57, s3, 0x2400
	s_cmp_ge_u32 s3, 3
	s_cselect_b32 s58, 0x9c00, 0
	s_add_u32 s57, s57, s58
	v_add_u32_e32 v37, s57, v1
	s_lshl_b32 s3, s20, 2
	s_add_u32 s3, s3, 3
	s_mul_i32 s57, s3, 0x2400
	s_cmp_ge_u32 s3, 3
	s_cselect_b32 s58, 0x9c00, 0
	s_add_u32 s57, s57, s58
	v_add_u32_e32 v38, s57, v1
	ds_write_b128 v36, v[40:43] offset:3072
	ds_write_b128 v36, v[56:59] offset:4096
	ds_write_b128 v36, v[72:75] offset:5120
	ds_write_b128 v37, v[44:47] offset:3072
	ds_write_b128 v37, v[60:63] offset:4096
	ds_write_b128 v37, v[76:79] offset:5120
	ds_write_b128 v38, v[52:55] offset:6144
	ds_write_b128 v38, v[68:71] offset:7168
	ds_write_b128 v38, v[84:87] offset:8192
	s_waitcnt lgkmcnt(0)
	s_barrier
	s_mov_b32 s3, s16
	s_mul_i32 s57, s3, 0x2400
	s_cmp_ge_u32 s3, 3
	s_cselect_b32 s58, 0x9c00, 0
	s_add_u32 s57, s57, s58
	v_add_u32_e32 v36, s57, v1
	ds_read_b128 v[88:91], v36 offset:0
	ds_read_b128 v[92:95], v36 offset:1024
	ds_read_b128 v[96:99], v36 offset:2048
	ds_read_b128 v[100:103], v36 offset:3072
	ds_read_b128 v[104:107], v36 offset:4096
	ds_read_b128 v[108:111], v36 offset:5120
	ds_read_b128 v[112:115], v36 offset:6144
	ds_read_b128 v[116:119], v36 offset:7168
	ds_read_b128 v[120:123], v36 offset:8192
	s_waitcnt lgkmcnt(0)
	v_add_f32_e32 v40, v48, v88
	v_add_f32_e32 v41, v49, v89
	v_add_f32_e32 v42, v50, v90
	v_add_f32_e32 v43, v51, v91
	v_add_f32_e32 v40, v40, v100
	v_add_f32_e32 v41, v41, v101
	v_add_f32_e32 v42, v42, v102
	v_add_f32_e32 v43, v43, v103
	v_add_f32_e32 v40, v40, v112
	v_add_f32_e32 v41, v41, v113
	v_add_f32_e32 v42, v42, v114
	v_add_f32_e32 v43, v43, v115
	v_add_f32_e32 v44, v64, v92
	v_add_f32_e32 v45, v65, v93
	v_add_f32_e32 v46, v66, v94
	v_add_f32_e32 v47, v67, v95
	v_add_f32_e32 v44, v44, v104
	v_add_f32_e32 v45, v45, v105
	v_add_f32_e32 v46, v46, v106
	v_add_f32_e32 v47, v47, v107
	v_add_f32_e32 v44, v44, v116
	v_add_f32_e32 v45, v45, v117
	v_add_f32_e32 v46, v46, v118
	v_add_f32_e32 v47, v47, v119
	v_add_f32_e32 v48, v80, v96
	v_add_f32_e32 v49, v81, v97
	v_add_f32_e32 v50, v82, v98
	v_add_f32_e32 v51, v83, v99
	v_add_f32_e32 v48, v48, v108
	v_add_f32_e32 v49, v49, v109
	v_add_f32_e32 v50, v50, v110
	v_add_f32_e32 v51, v51, v111
	v_add_f32_e32 v48, v48, v120
	v_add_f32_e32 v49, v49, v121
	v_add_f32_e32 v50, v50, v122
	v_add_f32_e32 v51, v51, v123
	s_branch .Lgm_red_done
.Lgm_red_not2:
	s_lshl_b32 s3, s20, 2
	s_mul_i32 s57, s3, 0x2400
	s_cmp_ge_u32 s3, 3
	s_cselect_b32 s58, 0x9c00, 0
	s_add_u32 s57, s57, s58
	v_add_u32_e32 v36, s57, v1
	s_lshl_b32 s3, s20, 2
	s_add_u32 s3, s3, 1
	s_mul_i32 s57, s3, 0x2400
	s_cmp_ge_u32 s3, 3
	s_cselect_b32 s58, 0x9c00, 0
	s_add_u32 s57, s57, s58
	v_add_u32_e32 v37, s57, v1
	s_lshl_b32 s3, s20, 2
	s_add_u32 s3, s3, 2
	s_mul_i32 s57, s3, 0x2400
	s_cmp_ge_u32 s3, 3
	s_cselect_b32 s58, 0x9c00, 0
	s_add_u32 s57, s57, s58
	v_add_u32_e32 v38, s57, v1
	ds_write_b128 v36, v[40:43] offset:6144
	ds_write_b128 v36, v[56:59] offset:7168
	ds_write_b128 v36, v[72:75] offset:8192
	ds_write_b128 v37, v[44:47] offset:6144
	ds_write_b128 v37, v[60:63] offset:7168
	ds_write_b128 v37, v[76:79] offset:8192
	ds_write_b128 v38, v[48:51] offset:6144
	ds_write_b128 v38, v[64:67] offset:7168
	ds_write_b128 v38, v[80:83] offset:8192
	s_waitcnt lgkmcnt(0)
	s_barrier
	s_mov_b32 s3, s16
	s_mul_i32 s57, s3, 0x2400
	s_cmp_ge_u32 s3, 3
	s_cselect_b32 s58, 0x9c00, 0
	s_add_u32 s57, s57, s58
	v_add_u32_e32 v36, s57, v1
	ds_read_b128 v[88:91], v36 offset:0
	ds_read_b128 v[92:95], v36 offset:1024
	ds_read_b128 v[96:99], v36 offset:2048
	ds_read_b128 v[100:103], v36 offset:3072
	ds_read_b128 v[104:107], v36 offset:4096
	ds_read_b128 v[108:111], v36 offset:5120
	ds_read_b128 v[112:115], v36 offset:6144
	ds_read_b128 v[116:119], v36 offset:7168
	ds_read_b128 v[120:123], v36 offset:8192
	s_waitcnt lgkmcnt(0)
	v_add_f32_e32 v40, v52, v88
	v_add_f32_e32 v41, v53, v89
	v_add_f32_e32 v42, v54, v90
	v_add_f32_e32 v43, v55, v91
	v_add_f32_e32 v40, v40, v100
	v_add_f32_e32 v41, v41, v101
	v_add_f32_e32 v42, v42, v102
	v_add_f32_e32 v43, v43, v103
	v_add_f32_e32 v40, v40, v112
	v_add_f32_e32 v41, v41, v113
	v_add_f32_e32 v42, v42, v114
	v_add_f32_e32 v43, v43, v115
	v_add_f32_e32 v44, v68, v92
	v_add_f32_e32 v45, v69, v93
	v_add_f32_e32 v46, v70, v94
	v_add_f32_e32 v47, v71, v95
	v_add_f32_e32 v44, v44, v104
	v_add_f32_e32 v45, v45, v105
	v_add_f32_e32 v46, v46, v106
	v_add_f32_e32 v47, v47, v107
	v_add_f32_e32 v44, v44, v116
	v_add_f32_e32 v45, v45, v117
	v_add_f32_e32 v46, v46, v118
	v_add_f32_e32 v47, v47, v119
	v_add_f32_e32 v48, v84, v96
	v_add_f32_e32 v49, v85, v97
	v_add_f32_e32 v50, v86, v98
	v_add_f32_e32 v51, v87, v99
	v_add_f32_e32 v48, v48, v108
	v_add_f32_e32 v49, v49, v109
	v_add_f32_e32 v50, v50, v110
	v_add_f32_e32 v51, v51, v111
	v_add_f32_e32 v48, v48, v120
	v_add_f32_e32 v49, v49, v121
	v_add_f32_e32 v50, v50, v122
	v_add_f32_e32 v51, v51, v123
.Lgm_red_done:
	v_cmp_eq_f32_e64 s[60:61], 0, v48
	v_cmp_eq_f32_e64 s[62:63], 0, v49
	v_cmp_eq_f32_e64 s[64:65], 0, v50
	v_cmp_eq_f32_e64 s[66:67], 0, v51
	s_nop 3
	s_or_b64 s[60:61], s[60:61], s[62:63]
	s_or_b64 s[64:65], s[64:65], s[66:67]
	s_or_b64 s[60:61], s[60:61], s[64:65]
	s_cmp_eq_u64 s[60:61], 0
	s_cbranch_scc1 .Lgm_no_fallback
	v_and_b32_e32 v101, 31, v2
	v_lshlrev_b32_e32 v101, 4, v101
	v_mov_b32_e32 v88, 0
	v_mov_b32_e32 v89, 0
	s_mov_b32 s3, 0
